# same fold in layer 0: softmax scale into the q gain of the layer-0 QK-norm phase, gqa16 QK accumulators start at -m*C, no per-score fma in the gqa16 tile loop
# speedup vs baseline: 1.0145x; 1.0045x over previous
; template <int NQ, int NK, bool CTXQ, bool GATES>
; __device__ __forceinline__ void phase_qknorm(const Args& a, int lane, int wave, int bid, int G, int ld, int qcol0, int kcol0, const float* qg, const float* kg) {
;     ...
;     const float q0 = qg[2 * lane], q1 = qg[2 * lane + 1], k0 = kg[2 * lane], k1 = kg[2 * lane + 1];
;     for (int t = gw; t < NTOK; t += NGW) {
;         const bool lat = t < SEQ; unsigned* base = (unsigned*)(P + (size_t)t * ld) + lane;
;         float c = 1.f, s = 0.f;
;         if (lat) { const int pos = lane < 32 ? (t >> 6) : (t & 63); const float* tp = TAB + 2 * (pos * 32 + (lane & 31)); c = tp[0]; s = tp[1]; }
; __global__ void __launch_bounds__(NWAVES * 64, 2) __attribute__((amdgpu_num_vgpr(248))) mega_fwd(Args args) {
;     ...
;         const float mraw = 128.0f * wave_max(fmaxf(fabsf(la.in[I_EVQG][lane]), fabsf(la.in[I_EVQG][64 + lane]))) * wave_max(fmaxf(fabsf(la.in[I_EVKG][lane]), fabsf(la.in[I_EVKG][64 + lane])));
;         const bool fixm = 2.0f * mraw * att::SCALE < 80.0f;
.LBB0_273:
	s_cmpk_gt_i32 s0, 0x40ff
	s_cbranch_scc1 .LBB0_278
	v_lshlrev_b32_e32 v7, 3, v1
	global_load_dwordx2 v[2:3], v7, s[16:17]
	s_waitcnt lgkmcnt(0)
	global_load_dwordx2 v[4:5], v7, s[18:19]
	v_lshlrev_b32_e32 v7, 1, v1
	v_cmp_gt_u32_e64 s[4:5], 32, v1
	v_and_b32_e32 v1, 62, v7
	v_mbcnt_lo_u32_b32 v7, -1, 0
	v_mbcnt_hi_u32_b32 v7, -1, v7
	v_and_b32_e32 v8, 64, v7
	v_add_u32_e32 v8, 64, v8
	v_xor_b32_e32 v9, 1, v7
	v_cmp_lt_i32_e32 vcc, v9, v8
	s_add_u32 s12, s22, 0x100000
	s_addc_u32 s13, s23, 0
	v_cndmask_b32_e32 v9, v7, v9, vcc
	v_lshlrev_b32_e32 v10, 2, v9
	v_xor_b32_e32 v9, 2, v7
	v_cmp_lt_i32_e32 vcc, v9, v8
	s_ashr_i32 s6, s3, 31
	s_add_u32 s2, s2, s3
	v_cndmask_b32_e32 v9, v7, v9, vcc
	v_lshlrev_b32_e32 v11, 2, v9
	v_xor_b32_e32 v9, 4, v7
	v_cmp_lt_i32_e32 vcc, v9, v8
	s_addc_u32 s3, 0, s6
	s_mulk_i32 s3, 0x2400
	v_cndmask_b32_e32 v9, v7, v9, vcc
	v_lshlrev_b32_e32 v12, 2, v9
	v_xor_b32_e32 v9, 8, v7
	v_cmp_lt_i32_e32 vcc, v9, v8
	s_mul_hi_u32 s6, s2, 0x2400
	s_add_i32 s6, s6, s3
	v_cndmask_b32_e32 v9, v7, v9, vcc
	v_lshlrev_b32_e32 v13, 2, v9
	v_xor_b32_e32 v9, 16, v7
	v_cmp_lt_i32_e32 vcc, v9, v8
	s_mulk_i32 s2, 0x2400
	s_add_u32 s2, s22, s2
	v_cndmask_b32_e32 v9, v7, v9, vcc
	v_lshlrev_b32_e32 v14, 2, v9
	v_xor_b32_e32 v9, 32, v7
	v_cmp_lt_i32_e32 vcc, v9, v8
	s_addc_u32 s3, s23, s6
	s_mul_hi_i32 s15, s1, 0x2400
	v_cndmask_b32_e32 v7, v7, v9, vcc
	v_lshlrev_b32_e32 v15, 2, v7
	v_mov_b32_e32 v7, 0
	v_lshl_add_u64 v[6:7], s[2:3], 0, v[6:7]
	s_mov_b64 s[2:3], 0x36552900
	v_lshl_add_u64 v[6:7], v[6:7], 0, s[2:3]
	s_mul_i32 s14, s1, 0x2400
	v_mov_b32_e32 v16, 0x358637bd
	s_mov_b32 s2, 0xf800000
	v_mov_b32_e32 v17, 0x260
	s_waitcnt vmcnt(0)
	v_max_f32_e64 v60, |v2|, |v3|
	v_max_f32_e64 v61, |v4|, |v5|
	ds_bpermute_b32 v62, v10, v60
	ds_bpermute_b32 v63, v10, v61
	s_waitcnt lgkmcnt(0)
	v_max_f32_e32 v60, v60, v62
	v_max_f32_e32 v61, v61, v63
	ds_bpermute_b32 v62, v11, v60
	ds_bpermute_b32 v63, v11, v61
	s_waitcnt lgkmcnt(0)
	v_max_f32_e32 v60, v60, v62
	v_max_f32_e32 v61, v61, v63
	ds_bpermute_b32 v62, v12, v60
	ds_bpermute_b32 v63, v12, v61
	s_waitcnt lgkmcnt(0)
	v_max_f32_e32 v60, v60, v62
	v_max_f32_e32 v61, v61, v63
	ds_bpermute_b32 v62, v13, v60
	ds_bpermute_b32 v63, v13, v61
	s_waitcnt lgkmcnt(0)
	v_max_f32_e32 v60, v60, v62
	v_max_f32_e32 v61, v61, v63
	ds_bpermute_b32 v62, v14, v60
	ds_bpermute_b32 v63, v14, v61
	s_waitcnt lgkmcnt(0)
	v_max_f32_e32 v60, v60, v62
	v_max_f32_e32 v61, v61, v63
	ds_bpermute_b32 v62, v15, v60
	ds_bpermute_b32 v63, v15, v61
	s_waitcnt lgkmcnt(0)
	v_max_f32_e32 v60, v60, v62
	v_max_f32_e32 v61, v61, v63
	v_mul_f32_e32 v60, 0x43000000, v60
	v_mul_f32_e32 v60, v60, v61
	v_add_f32_e32 v60, v60, v60
	v_mul_f32_e32 v60, 0x3db504f3, v60
	v_mov_b32_e32 v62, 0x3e0293ee
	v_mov_b32_e32 v63, 1.0
	v_cmp_gt_f32_e32 vcc, 0x42a00000, v60
	v_cndmask_b32_e32 v62, v63, v62, vcc
	v_mul_f32_e32 v2, v2, v62
	v_mul_f32_e32 v3, v3, v62
	s_branch .LBB0_276

; template <int LDQ, int LDK, int LDO>
; __device__ __forceinline__ void attn_gqa16_body(const bf16* __restrict__ Qb, const bf16* __restrict__ Kh, const bf16* __restrict__ Vh, bf16* __restrict__ Ob, int seq, char* lds, float mref) {
;   const int tid = threadIdx.x, wid = tid >> 6, lane = tid & 63, l16 = lane & 15, g = lane >> 4;
;   char* V_lds = lds; char* K_lds = lds + G16_OFF_K;
;   constexpr float C = SCALE * 1.4426950408889634f; const float mnC = -mref * C;
;   float ls0 = 0.f, ls1 = 0.f; f32x4a o[8][2] = {}; bf16x8 qr[2][4];
;   { int l16q = l16, gq = g, widq = wid; asm volatile("" : "+v"(l16q), "+v"(gq), "+v"(widq));
;     const bf16* Qw = Qb + (widq >> 2) * 128 + (long)((widq & 3) * QBLK + l16q) * LDQ + gq * 8;
; #pragma unroll
;     for (int qt = 0; qt < 2; ++qt)
; #pragma unroll
;       for (int ds = 0; ds < 4; ++ds) qr[qt][ds] = *reinterpret_cast<const bf16x8*>(Qw + (long)qt * 16 * LDQ + ds * 32); }
;   const int sr = tid >> 4, sc = (tid & 15) * 8;
;   const int vst0 = (sc >> 4) * VP16 + sr * 32 + ((sc >> 3) & 1) * 16, vst1 = vst0 + 1024;
;   const int vb0 = (int)(uintptr_t)V_lds + (4 * g + (l16 >> 2)) * 32 + (l16 & 3) * 8;
;   const int kb0 = l16 * 272 + g * 16;
;   bf16x8 sv0, sv1, sk0, sk1;
;   const unsigned koff0 = (unsigned)(sr * LDK + sc) * 2u, koff1 = koff0 + 32u * LDK * 2u;
.LBB0_638:
	s_andn2_saveexec_b64 s[6:7], s[30:31]
	s_cbranch_execz .LBB0_652
	s_and_b64 vcc, exec, s[4:5]
	s_cbranch_vccnz .LBB0_652
	v_lshrrev_b32_e32 v3, 4, v5
	v_lshlrev_b32_e32 v5, 5, v1
	s_movk_i32 s0, 0x820
	v_mad_u32_u24 v3, v3, s0, v5
	v_and_b32_e32 v180, 15, v0
	v_and_or_b32 v3, v4, 16, v3
	v_lshlrev_b32_e32 v8, 3, v0
	v_lshlrev_b32_e32 v6, 4, v176
	v_add_u32_e32 v181, 0, v3
	v_mul_u32_u24_e32 v3, 0x110, v180
	s_cmp_lg_u32 0, -1
	v_add3_u32 v182, 0, v6, v3
	v_and_b32_e32 v3, 0x60, v8
	s_cselect_b32 s0, 0, 0
	v_add_u32_e32 v3, s0, v3
	s_movk_i32 s0, 0xff
	v_cmp_lt_u32_e64 s[4:5], s0, v0
	s_add_u32 s0, s28, 0x3f552400
	s_addc_u32 s1, s29, 0
	s_add_u32 s2, s28, 0x3f552c00
	s_addc_u32 s18, s29, 0
	s_add_u32 s19, s28, 0x3f552e00
	s_addc_u32 s20, s29, 0
	s_add_u32 s21, s28, 0x36552c00
	v_lshlrev_b32_e32 v4, 7, v176
	v_and_b32_e32 v5, 24, v8
	s_addc_u32 s22, s29, 0
	v_lshlrev_b32_e32 v2, 1, v2
	v_add3_u32 v183, v3, v5, v4
	s_add_u32 s23, s28, 0x36552e00
	v_lshl_add_u32 v2, v180, 4, v2
	v_mov_b32_e32 v3, 0
	s_mov_b32 s9, 0
	v_add_u32_e32 v184, 0x4100, v183
	v_lshrrev_b32_e32 v185, 6, v0
	v_mul_f32_e32 v186, 0xbe0293ee, v7
	v_mov_b32_e32 v248, v186
	v_mov_b32_e32 v249, v186
	v_mov_b32_e32 v250, v186
	v_mov_b32_e32 v251, v186
	s_addc_u32 s24, s29, 0
	v_lshl_add_u64 v[154:155], s[28:29], 0, v[2:3]
	s_mov_b32 s25, 0x120000
	s_movk_i32 s26, 0x2400
	s_mov_b32 s27, 0x24000
	s_mov_b32 s28, 0x48000
	s_mov_b32 s29, 0x90000
	s_mov_b32 s30, 0xd8000
	s_mov_b32 s31, 0x168000
	s_mov_b32 s34, 0x1b0000
	s_mov_b32 s36, 0x1f8000
	s_mov_b32 s37, 0x36702000
	s_mov_b32 s38, 0x3674a000
	s_mov_b32 s39, 0x36672000
	s_mov_b32 s40, 0x366ba000
	s_movk_i32 s41, 0x7fff
	s_mov_b32 s44, 0x10000
	v_mov_b32_e32 v187, 1
	s_mov_b32 s45, s94
	v_and_b32_e32 v253, 63, v0
	v_lshrrev_b32_e32 v252, 1, v253
	v_mul_u32_u24_e32 v252, 0x2400, v252
	v_and_b32_e32 v253, 1, v253
	v_lshl_add_u32 v252, v253, 4, v252
	v_lshrrev_b32_e32 v253, 6, v0
	v_lshl_add_u32 v253, v253, 5, v252
	v_lshrrev_b32_e32 v252, 6, v0
	v_mul_u32_u24_e32 v252, 0x820, v252
	s_nop 0
	v_readfirstlane_b32 s84, v252
	s_nop 3
	s_add_i32 s86, s84, 0x4100
	s_branch .LBB0_642

; #define HLOADV(kt) do { const char* vb_ = (const char*)Vh + (size_t)(kt) * (64 * LDK * 2); sv0 = *(const bf16x8*)(vb_ + koff0); sv1 = *(const bf16x8*)(vb_ + koff1); } while (0)
; #define HLOADK(kt) do { const char* kb_ = (const char*)Kh + (size_t)(kt) * (64 * LDK * 2); sk0 = *(const bf16x8*)(kb_ + koff0); sk1 = *(const bf16x8*)(kb_ + koff1); } while (0)
; #define HWRITEV(b) do { char* d_ = V_lds + (b) * G16_V; *(bf16x8*)(d_ + vst0) = sv0; *(bf16x8*)(d_ + vst1) = sv1; } while (0)
; #define HWRITEK(b) do { char* d_ = K_lds + (b) * GB_K; *(bf16x8*)(d_ + KSWZ(sr, sc * 2)) = sk0; *(bf16x8*)(d_ + KSWZ(32 + sr, sc * 2)) = sk1; } while (0)
; #define HEXP() do { _Pragma("unroll") for (int kt = 0; kt < 4; ++kt) { _Pragma("unroll") for (int qt = 0; qt < 2; ++qt) { _Pragma("unroll") for (int i = 0; i < 4; ++i) s[kt][qt][i] = __builtin_amdgcn_exp2f(fmaf(s[kt][qt][i], C, mnC)); } } } while (0)
; template <int LDQ, int LDK, int LDO>
; __device__ __forceinline__ void attn_gqa16_body(const bf16* __restrict__ Qb, const bf16* __restrict__ Kh, const bf16* __restrict__ Vh, bf16* __restrict__ Ob, int seq, char* lds, float mref) {
;     ...
;   { int l16q = l16, gq = g, widq = wid; asm volatile("" : "+v"(l16q), "+v"(gq), "+v"(widq));
;     const bf16* Qw = Qb + (widq >> 2) * 128 + (long)((widq & 3) * QBLK + l16q) * LDQ + gq * 8;
; #pragma unroll
;     for (int qt = 0; qt < 2; ++qt)
; #pragma unroll
;       for (int ds = 0; ds < 4; ++ds) qr[qt][ds] = *reinterpret_cast<const bf16x8*>(Qw + (long)qt * 16 * LDQ + ds * 32); }
;   const int sr = tid >> 4, sc = (tid & 15) * 8;
;   const int vst0 = (sc >> 4) * VP16 + sr * 32 + ((sc >> 3) & 1) * 16, vst1 = vst0 + 1024;
;   const int vb0 = (int)(uintptr_t)V_lds + (4 * g + (l16 >> 2)) * 32 + (l16 & 3) * 8;
;   const int kb0 = l16 * 272 + g * 16;
;   bf16x8 sv0, sv1, sk0, sk1;
;   const unsigned koff0 = (unsigned)(sr * LDK + sc) * 2u, koff1 = koff0 + 32u * LDK * 2u;
;     ...
;   f32x4a s[4][2]; bf16x8 pb[2][2];
;     ...
;   const int NT = seq / KVBLK;
;   HLOADK(0); HLOADV(0); asm volatile("s_waitcnt vmcnt(0)" ::: "memory"); HWRITEK(0); HWRITEV(0);
;   HLOADK(1); asm volatile("s_waitcnt vmcnt(0)" ::: "memory"); HWRITEK(1); __syncthreads();
;   HLOADK(2); HLOADV(1);
;   HQK(0); HEXP();
.LBB0_642:
	s_cmpk_gt_i32 s45, 0x1ff
	s_mov_b64 s[14:15], -1
	s_waitcnt vmcnt(63) expcnt(7) lgkmcnt(15)
	s_barrier
	s_cbranch_scc0 .LBB0_646
	s_add_i32 s17, s45, 0xfffffe00
	s_and_b32 s16, s45, 1
	s_and_b32 s8, s17, 0x1fffffc
	s_and_b32 s12, s45, 2
	s_or_b32 s8, s8, s12
	s_mul_i32 s12, s16, 0x120000
	s_add_u32 s14, s0, s12
	s_addc_u32 s15, s1, 0
	s_lshl_b32 s8, s8, 7
	v_mov_b32_e32 v4, v176
	v_mov_b32_e32 v5, v180
	v_mov_b32_e32 v2, v185
	s_lshl_b64 s[12:13], s[8:9], 1
	s_add_u32 s14, s14, s12
	v_lshlrev_b32_e32 v6, 5, v2
	v_and_b32_e32 v2, 0xffffff80, v6
	s_addc_u32 s15, s15, s13
	v_ashrrev_i32_e32 v3, 31, v2
	v_and_b32_e32 v6, 0x60, v6
	s_lshl_b32 s8, s17, 6
	v_lshl_add_u64 v[2:3], v[2:3], 1, s[14:15]
	v_add_u32_e32 v5, v6, v5
	v_lshlrev_b32_e32 v4, 3, v4
	s_and_b32 s8, s8, 0xffffff00
	v_mad_i64_i32 v[2:3], s[14:15], v5, s26, v[2:3]
	v_ashrrev_i32_e32 v5, 31, v4
	s_add_u32 s46, s2, s8
	v_lshl_add_u64 v[6:7], v[4:5], 1, v[2:3]
	s_addc_u32 s47, s18, 0
	global_load_dwordx4 v[22:25], v[6:7], off
	global_load_dwordx4 v[18:21], v[6:7], off offset:64
	global_load_dwordx4 v[10:13], v[6:7], off offset:128
	global_load_dwordx4 v[2:5], v[6:7], off offset:192
	v_add_co_u32_e32 v6, vcc, s27, v6
	s_add_u32 s48, s19, s8
	s_nop 0
	v_addc_co_u32_e32 v7, vcc, 0, v7, vcc
	v_lshl_add_u64 v[98:99], s[46:47], 0, v[178:179]
	s_addc_u32 s49, s20, 0
	v_add_co_u32_e32 v38, vcc, s28, v98
	v_lshl_add_u64 v[156:157], s[48:49], 0, v[178:179]
	s_nop 0
	v_addc_co_u32_e32 v39, vcc, 0, v99, vcc
	v_add_co_u32_e32 v46, vcc, s28, v156
	global_load_dwordx4 v[30:33], v[6:7], off
	global_load_dwordx4 v[26:29], v[6:7], off offset:64
	global_load_dwordx4 v[14:17], v[6:7], off offset:128
	s_nop 0
	global_load_dwordx4 v[6:9], v[6:7], off offset:192
	v_addc_co_u32_e32 v47, vcc, 0, v157, vcc
	v_add_co_u32_e32 v50, vcc, s29, v98
	global_load_dwordx4 v[34:37], v[98:99], off
	s_nop 0
	global_load_dwordx4 v[38:41], v[38:39], off
	v_addc_co_u32_e32 v51, vcc, 0, v99, vcc
	v_add_co_u32_e32 v54, vcc, s30, v98
	global_load_dwordx4 v[42:45], v[156:157], off
	s_nop 0
	global_load_dwordx4 v[46:49], v[46:47], off
	s_waitcnt vmcnt(0)
	v_addc_co_u32_e32 v55, vcc, 0, v99, vcc
	global_load_dwordx4 v[50:53], v[50:51], off
	s_nop 0
	global_load_dwordx4 v[54:57], v[54:55], off
	s_waitcnt vmcnt(5)
	ds_write_b128 v194, v[34:37] offset:33280
	s_waitcnt vmcnt(4)
	ds_write_b128 v194, v[38:41] offset:41984
	s_waitcnt vmcnt(3)
	ds_write_b128 v181, v[42:45]
	s_waitcnt vmcnt(2)
	ds_write_b128 v181, v[46:49] offset:1024
	s_waitcnt vmcnt(0)
	s_waitcnt vmcnt(1)
	ds_write_b128 v194, v[50:53] offset:50688
	s_waitcnt vmcnt(0)
	ds_write_b128 v194, v[54:57] offset:59392
	s_waitcnt lgkmcnt(0)
	s_barrier
	ds_read_b128 v[34:37], v182 offset:33280
	ds_read_b128 v[38:41], v182 offset:33344
	ds_read_b128 v[46:49], v182 offset:37632
	ds_read_b128 v[50:53], v182 offset:37696
	ds_read_b128 v[58:61], v182 offset:41984
	ds_read_b128 v[62:65], v182 offset:42048
	ds_read_b128 v[70:73], v182 offset:46336
	ds_read_b128 v[74:77], v182 offset:46400
	s_waitcnt lgkmcnt(7)
	v_mfma_f32_16x16x32_bf16 v[42:45], v[34:37], v[22:25], 0
	v_mfma_f32_16x16x32_bf16 v[34:37], v[34:37], v[30:33], 0
	s_waitcnt lgkmcnt(5)
	v_mfma_f32_16x16x32_bf16 v[54:57], v[46:49], v[22:25], 0
	v_mfma_f32_16x16x32_bf16 v[46:49], v[46:49], v[30:33], 0
	s_waitcnt lgkmcnt(3)
	v_mfma_f32_16x16x32_bf16 v[66:69], v[58:61], v[22:25], 0
	v_mfma_f32_16x16x32_bf16 v[58:61], v[58:61], v[30:33], 0
	s_waitcnt lgkmcnt(1)
	v_mfma_f32_16x16x32_bf16 v[78:81], v[70:73], v[22:25], 0
	v_mfma_f32_16x16x32_bf16 v[70:73], v[70:73], v[30:33], 0
	v_mfma_f32_16x16x32_bf16 v[42:45], v[38:41], v[18:21], v[42:45]
	v_mfma_f32_16x16x32_bf16 v[34:37], v[38:41], v[26:29], v[34:37]
	v_mfma_f32_16x16x32_bf16 v[38:41], v[50:53], v[18:21], v[54:57]
	v_mfma_f32_16x16x32_bf16 v[46:49], v[50:53], v[26:29], v[46:49]
	v_mfma_f32_16x16x32_bf16 v[50:53], v[62:65], v[18:21], v[66:69]
	v_mfma_f32_16x16x32_bf16 v[54:57], v[62:65], v[26:29], v[58:61]
	s_waitcnt lgkmcnt(0)
	v_mfma_f32_16x16x32_bf16 v[62:65], v[74:77], v[26:29], v[70:73]
	ds_read_b128 v[66:69], v182 offset:33408
	s_nop 1
	ds_read_b128 v[70:73], v182 offset:33472
	v_mfma_f32_16x16x32_bf16 v[58:61], v[74:77], v[18:21], v[78:81]
	s_waitcnt lgkmcnt(1)
	v_mfma_f32_16x16x32_bf16 v[42:45], v[66:69], v[10:13], v[42:45]
	v_mfma_f32_16x16x32_bf16 v[34:37], v[66:69], v[14:17], v[34:37]
	ds_read_b128 v[66:69], v182 offset:37760
	ds_read_b128 v[74:77], v182 offset:37824
	s_waitcnt lgkmcnt(1)
	v_mfma_f32_16x16x32_bf16 v[38:41], v[66:69], v[10:13], v[38:41]
	v_mfma_f32_16x16x32_bf16 v[46:49], v[66:69], v[14:17], v[46:49]
	ds_read_b128 v[66:69], v182 offset:42112
	ds_read_b128 v[78:81], v182 offset:42176
	s_waitcnt lgkmcnt(1)
	v_mfma_f32_16x16x32_bf16 v[90:93], v[66:69], v[10:13], v[50:53]
	s_nop 2
	ds_read_b128 v[50:53], v182 offset:46464
	ds_read_b128 v[100:103], v182 offset:46528
	s_waitcnt lgkmcnt(1)
	v_mfma_f32_16x16x32_bf16 v[94:97], v[50:53], v[10:13], v[58:61]
	v_mfma_f32_16x16x32_bf16 v[58:61], v[70:73], v[6:9], v[34:37]
	s_nop 2
	v_add_co_u32_e32 v34, vcc, s25, v98
	v_mfma_f32_16x16x32_bf16 v[66:69], v[66:69], v[14:17], v[54:57]
	s_nop 0
	v_addc_co_u32_e32 v35, vcc, 0, v99, vcc
	v_add_co_u32_e32 v36, vcc, s31, v98
	v_mfma_f32_16x16x32_bf16 v[104:107], v[50:53], v[14:17], v[62:65]
	s_nop 0
	v_addc_co_u32_e32 v37, vcc, 0, v99, vcc
	global_load_dwordx4 v[82:85], v[34:35], off
	global_load_dwordx4 v[86:89], v[36:37], off
	v_add_co_u32_e32 v34, vcc, s29, v156
	v_mfma_f32_16x16x32_bf16 v[54:57], v[74:77], v[2:5], v[38:41]
	s_nop 0
	v_addc_co_u32_e32 v35, vcc, 0, v157, vcc
	v_add_co_u32_e32 v36, vcc, s30, v156
	v_mfma_f32_16x16x32_bf16 v[50:53], v[74:77], v[6:9], v[46:49]
	s_nop 0
	v_addc_co_u32_e32 v37, vcc, 0, v157, vcc
	v_mfma_f32_16x16x32_bf16 v[46:49], v[78:81], v[2:5], v[90:93]
	s_waitcnt lgkmcnt(0)
; #define HLOADV(kt) do { const char* vb_ = (const char*)Vh + (size_t)(kt) * (64 * LDK * 2); sv0 = *(const bf16x8*)(vb_ + koff0); sv1 = *(const bf16x8*)(vb_ + koff1); } while (0)
; #define HLOADK(kt) do { const char* kb_ = (const char*)Kh + (size_t)(kt) * (64 * LDK * 2); sk0 = *(const bf16x8*)(kb_ + koff0); sk1 = *(const bf16x8*)(kb_ + koff1); } while (0)
; #define HWRITEV(b) do { char* d_ = V_lds + (b) * G16_V; *(bf16x8*)(d_ + vst0) = sv0; *(bf16x8*)(d_ + vst1) = sv1; } while (0)
; #define HWRITEK(b) do { char* d_ = K_lds + (b) * GB_K; *(bf16x8*)(d_ + KSWZ(sr, sc * 2)) = sk0; *(bf16x8*)(d_ + KSWZ(32 + sr, sc * 2)) = sk1; } while (0)
; #define HEXP() do { _Pragma("unroll") for (int kt = 0; kt < 4; ++kt) { _Pragma("unroll") for (int qt = 0; qt < 2; ++qt) { _Pragma("unroll") for (int i = 0; i < 4; ++i) s[kt][qt][i] = __builtin_amdgcn_exp2f(fmaf(s[kt][qt][i], C, mnC)); } } } while (0)
; template <int LDQ, int LDK, int LDO>
; __device__ __forceinline__ void attn_gqa16_body(const bf16* __restrict__ Qb, const bf16* __restrict__ Kh, const bf16* __restrict__ Vh, bf16* __restrict__ Ob, int seq, char* lds, float mref) {
;     ...
;   const int NT = seq / KVBLK;
;   HLOADK(0); HLOADV(0); asm volatile("s_waitcnt vmcnt(0)" ::: "memory"); HWRITEK(0); HWRITEV(0);
;   HLOADK(1); asm volatile("s_waitcnt vmcnt(0)" ::: "memory"); HWRITEK(1); __syncthreads();
;   HLOADK(2); HLOADV(1);
;   HQK(0); HEXP();
;   if (wid >= 4) __builtin_amdgcn_s_setprio(1);
;   for (int t = 0; t < NT; ++t) {
;     HPACK();
;     __syncthreads();
;     const bool more = t + 1 < NT;
;     if (more) HQK((t + 1) & 1);
	v_mfma_f32_16x16x32_bf16 v[38:41], v[100:103], v[2:5], v[94:97]
	s_nop 0
	global_load_dwordx4 v[90:93], v[34:35], off
	s_nop 0
	global_load_dwordx4 v[94:97], v[36:37], off
	v_mfma_f32_16x16x32_bf16 v[62:65], v[70:73], v[2:5], v[42:45]
	v_mfma_f32_16x16x32_bf16 v[42:45], v[78:81], v[6:9], v[66:69]
	v_mfma_f32_16x16x32_bf16 v[34:37], v[100:103], v[6:9], v[104:107]
	s_and_saveexec_b64 s[14:15], s[4:5]
	s_setprio 1
	s_or_b64 exec, exec, s[14:15]
	s_nop 2
	v_add_f32_e32 v63, v186, v63
	v_exp_f32_e32 v66, v63
	v_add_f32_e32 v63, v186, v64
	v_exp_f32_e32 v64, v63
	v_add_f32_e32 v63, v186, v65
	v_add_f32_e32 v58, v186, v58
	v_add_f32_e32 v54, v186, v54
	v_add_f32_e32 v50, v186, v50
	v_add_f32_e32 v46, v186, v46
	v_add_f32_e32 v42, v186, v42
	v_add_f32_e32 v38, v186, v38
	v_add_f32_e32 v34, v186, v34
	v_exp_f32_e32 v80, v63
	v_exp_f32_e32 v63, v58
	v_add_f32_e32 v58, v186, v59
	v_exp_f32_e32 v112, v54
	v_add_f32_e32 v54, v186, v55
	v_exp_f32_e32 v113, v50
	v_add_f32_e32 v50, v186, v51
	v_exp_f32_e32 v136, v46
	v_add_f32_e32 v46, v186, v47
	v_exp_f32_e32 v137, v42
	v_add_f32_e32 v42, v186, v43
	v_exp_f32_e32 v152, v38
	v_add_f32_e32 v38, v186, v39
	v_exp_f32_e32 v153, v34
	v_add_f32_e32 v34, v186, v35
	v_exp_f32_e32 v67, v58
	v_add_f32_e32 v58, v186, v60
	v_exp_f32_e32 v130, v54
	v_add_f32_e32 v54, v186, v56
	v_exp_f32_e32 v131, v50
	v_add_f32_e32 v50, v186, v52
	v_exp_f32_e32 v138, v46
	v_add_f32_e32 v46, v186, v48
	v_exp_f32_e32 v139, v42
	v_add_f32_e32 v42, v186, v44
	v_exp_f32_e32 v170, v38
	v_add_f32_e32 v38, v186, v40
	v_exp_f32_e32 v171, v34
	v_add_f32_e32 v34, v186, v36
	v_add_f32_e32 v62, v186, v62
	v_exp_f32_e32 v65, v58
	v_add_f32_e32 v58, v186, v61
	v_exp_f32_e32 v132, v54
	v_add_f32_e32 v54, v186, v57
	v_exp_f32_e32 v133, v50
	v_add_f32_e32 v50, v186, v53
	v_exp_f32_e32 v140, v46
	v_add_f32_e32 v46, v186, v49
	v_exp_f32_e32 v141, v42
	v_add_f32_e32 v42, v186, v45
	v_exp_f32_e32 v172, v38
	v_add_f32_e32 v38, v186, v41
	v_exp_f32_e32 v173, v34
	v_add_f32_e32 v34, v186, v37
	v_exp_f32_e32 v62, v62
	v_exp_f32_e32 v81, v58
	v_exp_f32_e32 v134, v54
	v_exp_f32_e32 v135, v50
	v_exp_f32_e32 v142, v46
	v_exp_f32_e32 v143, v42
	v_exp_f32_e32 v174, v38
	v_exp_f32_e32 v175, v34
	v_cvt_pk_bf16_f32 v114, v62, v66
	v_cvt_pk_bf16_f32 v115, v64, v80
	v_cvt_pk_bf16_f32 v116, v112, v130
	v_cvt_pk_bf16_f32 v117, v132, v134
	v_cvt_pk_bf16_f32 v118, v63, v67
	v_cvt_pk_bf16_f32 v119, v65, v81
	v_cvt_pk_bf16_f32 v120, v113, v131
	v_cvt_pk_bf16_f32 v121, v133, v135
	v_cvt_pk_bf16_f32 v122, v136, v138
	v_cvt_pk_bf16_f32 v123, v140, v142
	v_cvt_pk_bf16_f32 v124, v152, v170
	v_cvt_pk_bf16_f32 v125, v172, v174
	v_cvt_pk_bf16_f32 v126, v137, v139
	v_cvt_pk_bf16_f32 v127, v141, v143
	v_cvt_pk_bf16_f32 v128, v153, v171
	v_cvt_pk_bf16_f32 v129, v173, v175
	s_barrier
	ds_read_b128 v[34:37], v182 offset:50688
	ds_read_b128 v[38:41], v182 offset:50752
	ds_read_b128 v[46:49], v182 offset:55040
	ds_read_b128 v[50:53], v182 offset:55104
	ds_read_b128 v[58:61], v182 offset:59392
	ds_read_b128 v[68:71], v182 offset:59456
	ds_read_b128 v[76:79], v182 offset:63744
	ds_read_b128 v[100:103], v182 offset:63808
	s_waitcnt lgkmcnt(7)
	v_mfma_f32_16x16x32_bf16 v[42:45], v[34:37], v[22:25], 0
	s_lshl_b32 s8, s16, 19
	s_add_u32 s8, s42, s8
	s_addc_u32 s14, s43, 0
	v_mfma_f32_16x16x32_bf16 v[34:37], v[34:37], v[30:33], 0
	s_add_u32 s8, s8, s12
	s_addc_u32 s13, s14, s13
	s_add_u32 s12, s8, 0x4000000
	s_waitcnt lgkmcnt(5)
	v_mfma_f32_16x16x32_bf16 v[54:57], v[46:49], v[22:25], 0
	s_addc_u32 s13, s13, 0
	v_mfma_f32_16x16x32_bf16 v[46:49], v[46:49], v[30:33], 0
	s_waitcnt lgkmcnt(3)
	v_mfma_f32_16x16x32_bf16 v[72:75], v[58:61], v[22:25], 0
	v_mfma_f32_16x16x32_bf16 v[58:61], v[58:61], v[30:33], 0
	s_waitcnt lgkmcnt(1)
	v_mfma_f32_16x16x32_bf16 v[104:107], v[76:79], v[22:25], 0
	v_mfma_f32_16x16x32_bf16 v[76:79], v[76:79], v[30:33], 0
	v_mfma_f32_16x16x32_bf16 v[42:45], v[38:41], v[18:21], v[42:45]
	v_mfma_f32_16x16x32_bf16 v[34:37], v[38:41], v[26:29], v[34:37]
	v_mfma_f32_16x16x32_bf16 v[38:41], v[50:53], v[18:21], v[54:57]
	v_mfma_f32_16x16x32_bf16 v[46:49], v[50:53], v[26:29], v[46:49]
	v_mfma_f32_16x16x32_bf16 v[50:53], v[68:71], v[18:21], v[72:75]
	v_mfma_f32_16x16x32_bf16 v[54:57], v[68:71], v[26:29], v[58:61]
	s_waitcnt lgkmcnt(0)
	v_mfma_f32_16x16x32_bf16 v[68:71], v[100:103], v[26:29], v[76:79]
	ds_read_b128 v[72:75], v182 offset:50816
	s_nop 1
	ds_read_b128 v[76:79], v182 offset:50880
	v_mfma_f32_16x16x32_bf16 v[58:61], v[100:103], v[18:21], v[104:107]
	s_waitcnt lgkmcnt(1)
	v_mfma_f32_16x16x32_bf16 v[42:45], v[72:75], v[10:13], v[42:45]
	v_mfma_f32_16x16x32_bf16 v[34:37], v[72:75], v[14:17], v[34:37]
	ds_read_b128 v[72:75], v182 offset:55168
	ds_read_b128 v[100:103], v182 offset:55232
	s_waitcnt lgkmcnt(1)
	v_mfma_f32_16x16x32_bf16 v[38:41], v[72:75], v[10:13], v[38:41]
	v_mfma_f32_16x16x32_bf16 v[46:49], v[72:75], v[14:17], v[46:49]
	ds_read_b128 v[72:75], v182 offset:59520
	ds_read_b128 v[104:107], v182 offset:59584
	s_waitcnt lgkmcnt(1)
	v_mfma_f32_16x16x32_bf16 v[50:53], v[72:75], v[10:13], v[50:53]
	v_mfma_f32_16x16x32_bf16 v[54:57], v[72:75], v[14:17], v[54:57]
	ds_read_b128 v[72:75], v182 offset:63872
	ds_read_b128 v[108:111], v182 offset:63936
	v_mfma_f32_16x16x32_bf16 v[148:151], v[76:79], v[6:9], v[34:37]
	s_nop 2
	v_add_f32_e64 v34, v62, v66
	v_add_f32_e64 v35, v63, v67
	v_pk_add_f32 v[36:37], v[64:65], v[80:81]
	s_waitcnt lgkmcnt(1)
; template <int D0> __device__ __forceinline__ void pv16(f32x4a (&o)[8][2], int vb, const bf16x8 (&pb)[2][2]) {
;     ...
;   const s16x4 a0 = TR(D0, 0, 0), a1 = TR(D0, 0, 1), a2 = TR(D0, 1, 0), a3 = TR(D0, 1, 1), b0 = TR(D0 + 1, 0, 0), b1 = TR(D0 + 1, 0, 1), b2 = TR(D0 + 1, 1, 0), b3 = TR(D0 + 1, 1, 1);
;   const s16x4 c0 = TR(D0 + 2, 0, 0), c1 = TR(D0 + 2, 0, 1), c2 = TR(D0 + 2, 1, 0), c3 = TR(D0 + 2, 1, 1);
;   asm volatile("s_waitcnt lgkmcnt(4)" ::: "memory"); SBAR();
;   o[D0][0] = MFMA16(PK16(a0, a1), pb[0][0], o[D0][0]); o[D0][1] = MFMA16(PK16(a0, a1), pb[0][1], o[D0][1]);
;   o[D0 + 1][0] = MFMA16(PK16(b0, b1), pb[0][0], o[D0 + 1][0]); o[D0 + 1][1] = MFMA16(PK16(b0, b1), pb[0][1], o[D0 + 1][1]);
;   o[D0][0] = MFMA16(PK16(a2, a3), pb[1][0], o[D0][0]); o[D0][1] = MFMA16(PK16(a2, a3), pb[1][1], o[D0][1]);
;   o[D0 + 1][0] = MFMA16(PK16(b2, b3), pb[1][0], o[D0 + 1][0]); o[D0 + 1][1] = MFMA16(PK16(b2, b3), pb[1][1], o[D0 + 1][1]);
;   SBAR();
;   const s16x4 d0 = TR(D0 + 3, 0, 0), d1 = TR(D0 + 3, 0, 1), d2 = TR(D0 + 3, 1, 0), d3 = TR(D0 + 3, 1, 1);
;   asm volatile("s_waitcnt lgkmcnt(4)" ::: "memory"); SBAR();
;   o[D0 + 2][0] = MFMA16(PK16(c0, c1), pb[0][0], o[D0 + 2][0]); o[D0 + 2][1] = MFMA16(PK16(c0, c1), pb[0][1], o[D0 + 2][1]);
;   o[D0 + 2][0] = MFMA16(PK16(c2, c3), pb[1][0], o[D0 + 2][0]); o[D0 + 2][1] = MFMA16(PK16(c2, c3), pb[1][1], o[D0 + 2][1]);
;   asm volatile("s_waitcnt lgkmcnt(0)" ::: "memory"); SBAR();
;   o[D0 + 3][0] = MFMA16(PK16(d0, d1), pb[0][0], o[D0 + 3][0]); o[D0 + 3][1] = MFMA16(PK16(d0, d1), pb[0][1], o[D0 + 3][1]);
;   o[D0 + 3][0] = MFMA16(PK16(d2, d3), pb[1][0], o[D0 + 3][0]); o[D0 + 3][1] = MFMA16(PK16(d2, d3), pb[1][1], o[D0 + 3][1]);
; template <int LDQ, int LDK, int LDO>
; __device__ __forceinline__ void attn_gqa16_body(const bf16* __restrict__ Qb, const bf16* __restrict__ Kh, const bf16* __restrict__ Vh, bf16* __restrict__ Ob, int seq, char* lds, float mref) {
;     ...
;   for (int t = 0; t < NT; ++t) {
;     HPACK();
;     __syncthreads();
;     const bool more = t + 1 < NT;
;     if (more) HQK((t + 1) & 1);
;     const int vb = vb0 + (t & 1) * (int)G16_V;
;     SBAR(); pv16<0>(o, vb, pb); SBAR();
;     asm volatile("s_waitcnt vmcnt(0)" ::: "memory");
;     if (t + 2 < NT) HWRITEK(t & 1);
;     if (t + 1 < NT) HWRITEV((t + 1) & 1);
;     HLOADK(t + 3); HLOADV(t + 2);
;     SBAR(); pv16<4>(o, vb, pb); SBAR();
	v_mfma_f32_16x16x32_bf16 v[58:61], v[72:75], v[10:13], v[58:61]
	v_add_f32_e64 v34, v34, v36
	v_add_f32_e64 v35, v35, v37
	v_pk_add_f32 v[36:37], v[112:113], v[130:131]
	v_pk_add_f32 v[34:35], v[34:35], 0 op_sel_hi:[1,0]
	v_mfma_f32_16x16x32_bf16 v[68:71], v[72:75], v[14:17], v[68:71]
	v_mfma_f32_16x16x32_bf16 v[158:161], v[100:103], v[2:5], v[38:41]
	s_nop 2
	v_add_f32_e64 v38, v132, v134
	v_add_f32_e64 v39, v133, v135
	v_pk_add_f32 v[40:41], v[140:141], v[142:143]
	v_pk_add_f32 v[36:37], v[36:37], v[38:39]
	v_pk_add_f32 v[38:39], v[136:137], v[138:139]
	v_mfma_f32_16x16x32_bf16 v[144:147], v[76:79], v[2:5], v[42:45]
	v_add_f32_e64 v38, v38, v40
	v_add_f32_e64 v39, v39, v41
	v_pk_add_f32 v[40:41], v[152:153], v[170:171]
	v_pk_add_f32 v[34:35], v[36:37], v[34:35]
	v_pk_add_f32 v[42:43], v[172:173], v[174:175]
	v_pk_add_f32 v[34:35], v[38:39], v[34:35]
	v_pk_add_f32 v[40:41], v[40:41], v[42:43]
	v_mfma_f32_16x16x32_bf16 v[162:165], v[100:103], v[6:9], v[46:49]
	v_add_f32_e64 v142, v40, v34
	v_add_f32_e64 v143, v41, v35
	v_mfma_f32_16x16x32_bf16 v[166:169], v[104:107], v[2:5], v[50:53]
	v_mfma_f32_16x16x32_bf16 v[138:141], v[104:107], v[6:9], v[54:57]
	s_waitcnt lgkmcnt(0)
	v_mfma_f32_16x16x32_bf16 v[134:137], v[108:111], v[2:5], v[58:61]
	v_mfma_f32_16x16x32_bf16 v[130:133], v[108:111], v[6:9], v[68:71]
	ds_read_b64_tr_b16 v[34:35], v183 offset:0
	ds_read_b64_tr_b16 v[36:37], v183 offset:0x200
	ds_read_b64_tr_b16 v[38:39], v183 offset:0x400
	ds_read_b64_tr_b16 v[40:41], v183 offset:0x600
	ds_read_b64_tr_b16 v[42:43], v183 offset:0x820
	ds_read_b64_tr_b16 v[44:45], v183 offset:0xa20
	ds_read_b64_tr_b16 v[46:47], v183 offset:0xc20
	ds_read_b64_tr_b16 v[48:49], v183 offset:0xe20
	ds_read_b64_tr_b16 v[50:51], v183 offset:0x1040
	ds_read_b64_tr_b16 v[52:53], v183 offset:0x1240
	ds_read_b64_tr_b16 v[54:55], v183 offset:0x1440
	ds_read_b64_tr_b16 v[56:57], v183 offset:0x1640
	s_waitcnt lgkmcnt(4)
	s_nop 0
	v_mfma_f32_16x16x32_bf16 v[58:61], v[34:37], v[114:117], 0
	v_mfma_f32_16x16x32_bf16 v[34:37], v[34:37], v[118:121], 0
	v_mfma_f32_16x16x32_bf16 v[62:65], v[42:45], v[114:117], 0
	v_mfma_f32_16x16x32_bf16 v[42:45], v[42:45], v[118:121], 0
	v_mfma_f32_16x16x32_bf16 v[66:69], v[38:41], v[122:125], v[58:61]
	v_mfma_f32_16x16x32_bf16 v[70:73], v[38:41], v[126:129], v[34:37]
	v_mfma_f32_16x16x32_bf16 v[74:77], v[46:49], v[122:125], v[62:65]
	v_mfma_f32_16x16x32_bf16 v[78:81], v[46:49], v[126:129], v[42:45]
	ds_read_b64_tr_b16 v[34:35], v183 offset:0x1860
	ds_read_b64_tr_b16 v[36:37], v183 offset:0x1a60
	ds_read_b64_tr_b16 v[38:39], v183 offset:0x1c60
	ds_read_b64_tr_b16 v[40:41], v183 offset:0x1e60
	s_waitcnt lgkmcnt(4)
	v_mfma_f32_16x16x32_bf16 v[42:45], v[50:53], v[114:117], 0
	s_waitcnt lgkmcnt(0)
	v_mfma_f32_16x16x32_bf16 v[50:53], v[50:53], v[118:121], 0
	v_mfma_f32_16x16x32_bf16 v[46:49], v[54:57], v[122:125], v[42:45]
	v_mfma_f32_16x16x32_bf16 v[62:65], v[54:57], v[126:129], v[50:53]
	v_mfma_f32_16x16x32_bf16 v[42:45], v[34:37], v[114:117], 0
	v_mfma_f32_16x16x32_bf16 v[34:37], v[34:37], v[118:121], 0
	v_mfma_f32_16x16x32_bf16 v[50:53], v[38:41], v[122:125], v[42:45]
	v_mfma_f32_16x16x32_bf16 v[54:57], v[38:41], v[126:129], v[34:37]
	s_nop 5
	v_add_co_u32_e32 v34, vcc, s34, v98
	s_waitcnt vmcnt(0)
	s_nop 1
	v_addc_co_u32_e32 v35, vcc, 0, v99, vcc
	v_add_co_u32_e32 v38, vcc, s36, v98
	s_nop 1
	v_addc_co_u32_e32 v39, vcc, 0, v99, vcc
	v_add_co_u32_e32 v42, vcc, s25, v156
	global_load_dwordx4 v[34:37], v[34:35], off
	s_nop 0
	global_load_dwordx4 v[38:41], v[38:39], off
	v_addc_co_u32_e32 v43, vcc, 0, v157, vcc
	v_add_co_u32_e32 v58, vcc, s31, v156
	s_nop 1
	v_addc_co_u32_e32 v59, vcc, 0, v157, vcc
	global_load_dwordx4 v[42:45], v[42:43], off
	s_nop 0
	global_load_dwordx4 v[58:61], v[58:59], off
	s_waitcnt vmcnt(7)
	ds_write_b128 v194, v[82:85] offset:33280
	s_waitcnt vmcnt(6)
	ds_write_b128 v194, v[86:89] offset:41984
	s_waitcnt vmcnt(5)
	ds_write_b128 v181, v[90:93] offset:16640
	s_waitcnt vmcnt(4)
	ds_write_b128 v181, v[94:97] offset:17664
	ds_read_b64_tr_b16 v[82:83], v183 offset:0x2080
	ds_read_b64_tr_b16 v[84:85], v183 offset:0x2280
	ds_read_b64_tr_b16 v[86:87], v183 offset:0x2480
	ds_read_b64_tr_b16 v[88:89], v183 offset:0x2680
	ds_read_b64_tr_b16 v[90:91], v183 offset:0x28a0
	ds_read_b64_tr_b16 v[92:93], v183 offset:0x2aa0
	ds_read_b64_tr_b16 v[94:95], v183 offset:0x2ca0
	ds_read_b64_tr_b16 v[96:97], v183 offset:0x2ea0
	ds_read_b64_tr_b16 v[170:171], v183 offset:0x30c0
	ds_read_b64_tr_b16 v[172:173], v183 offset:0x32c0
	ds_read_b64_tr_b16 v[196:197], v183 offset:0x34c0
	ds_read_b64_tr_b16 v[198:199], v183 offset:0x36c0
	s_waitcnt lgkmcnt(4)
	s_nop 0
	v_mfma_f32_16x16x32_bf16 v[98:101], v[82:85], v[114:117], 0
	v_mfma_f32_16x16x32_bf16 v[82:85], v[82:85], v[118:121], 0
	v_mfma_f32_16x16x32_bf16 v[106:109], v[90:93], v[114:117], 0
	v_mfma_f32_16x16x32_bf16 v[90:93], v[90:93], v[118:121], 0
	v_mfma_f32_16x16x32_bf16 v[98:101], v[86:89], v[122:125], v[98:101]
	v_mfma_f32_16x16x32_bf16 v[102:105], v[86:89], v[126:129], v[82:85]
	v_mfma_f32_16x16x32_bf16 v[106:109], v[94:97], v[122:125], v[106:109]
	v_mfma_f32_16x16x32_bf16 v[110:113], v[94:97], v[126:129], v[90:93]
	ds_read_b64_tr_b16 v[86:87], v183 offset:0x38e0
	ds_read_b64_tr_b16 v[88:89], v183 offset:0x3ae0
	ds_read_b64_tr_b16 v[90:91], v183 offset:0x3ce0
	ds_read_b64_tr_b16 v[92:93], v183 offset:0x3ee0
	s_waitcnt lgkmcnt(4)
	v_mfma_f32_16x16x32_bf16 v[82:85], v[170:173], v[114:117], 0
	s_waitcnt lgkmcnt(0)
; #define SBAR() __builtin_amdgcn_sched_barrier(0)
; #define HLOADV(kt) do { const char* vb_ = (const char*)Vh + (size_t)(kt) * (64 * LDK * 2); sv0 = *(const bf16x8*)(vb_ + koff0); sv1 = *(const bf16x8*)(vb_ + koff1); } while (0)
; #define HLOADK(kt) do { const char* kb_ = (const char*)Kh + (size_t)(kt) * (64 * LDK * 2); sk0 = *(const bf16x8*)(kb_ + koff0); sk1 = *(const bf16x8*)(kb_ + koff1); } while (0)
; #define HWRITEV(b) do { char* d_ = V_lds + (b) * G16_V; *(bf16x8*)(d_ + vst0) = sv0; *(bf16x8*)(d_ + vst1) = sv1; } while (0)
; #define HWRITEK(b) do { char* d_ = K_lds + (b) * GB_K; *(bf16x8*)(d_ + KSWZ(sr, sc * 2)) = sk0; *(bf16x8*)(d_ + KSWZ(32 + sr, sc * 2)) = sk1; } while (0)
; #define HEXP() do { _Pragma("unroll") for (int kt = 0; kt < 4; ++kt) { _Pragma("unroll") for (int qt = 0; qt < 2; ++qt) { _Pragma("unroll") for (int i = 0; i < 4; ++i) s[kt][qt][i] = __builtin_amdgcn_exp2f(fmaf(s[kt][qt][i], C, mnC)); } } } while (0)
; template <int LDQ, int LDK, int LDO>
; __device__ __forceinline__ void attn_gqa16_body(const bf16* __restrict__ Qb, const bf16* __restrict__ Kh, const bf16* __restrict__ Vh, bf16* __restrict__ Ob, int seq, char* lds, float mref) {
;     ...
;   const int NT = seq / KVBLK;
;   HLOADK(0); HLOADV(0); asm volatile("s_waitcnt vmcnt(0)" ::: "memory"); HWRITEK(0); HWRITEV(0);
;   HLOADK(1); asm volatile("s_waitcnt vmcnt(0)" ::: "memory"); HWRITEK(1); __syncthreads();
;   HLOADK(2); HLOADV(1);
;   HQK(0); HEXP();
;   if (wid >= 4) __builtin_amdgcn_s_setprio(1);
;   for (int t = 0; t < NT; ++t) {
;     HPACK();
;     __syncthreads();
;     const bool more = t + 1 < NT;
;     if (more) HQK((t + 1) & 1);
;     const int vb = vb0 + (t & 1) * (int)G16_V;
;     SBAR(); pv16<0>(o, vb, pb); SBAR();
	v_mfma_f32_16x16x32_bf16 v[94:97], v[170:173], v[118:121], 0
	v_mfma_f32_16x16x32_bf16 v[82:85], v[196:199], v[122:125], v[82:85]
	v_mfma_f32_16x16x32_bf16 v[94:97], v[196:199], v[126:129], v[94:97]
	v_mfma_f32_16x16x32_bf16 v[114:117], v[86:89], v[114:117], 0
	v_mfma_f32_16x16x32_bf16 v[118:121], v[86:89], v[118:121], 0
	v_mfma_f32_16x16x32_bf16 v[86:89], v[90:93], v[122:125], v[114:117]
	v_mfma_f32_16x16x32_bf16 v[90:93], v[90:93], v[126:129], v[118:121]
	s_nop 4
	v_add_f32_e32 v114, v186, v144
	v_exp_f32_e32 v152, v114
	v_add_f32_e32 v114, v186, v145
	v_exp_f32_e32 v174, v114
	v_add_f32_e32 v114, v186, v146
	v_exp_f32_e32 v190, v114
	v_add_f32_e32 v114, v186, v147
	v_exp_f32_e32 v192, v114
	v_add_f32_e32 v114, v186, v148
	v_exp_f32_e32 v153, v114
	v_add_f32_e32 v114, v186, v149
	v_exp_f32_e32 v175, v114
	v_add_f32_e32 v114, v186, v150
	v_exp_f32_e32 v191, v114
	v_add_f32_e32 v114, v186, v151
	v_exp_f32_e32 v193, v114
	v_add_f32_e32 v114, v186, v158
	v_exp_f32_e32 v216, v114
	v_add_f32_e32 v114, v186, v159
	v_exp_f32_e32 v218, v114
	v_add_f32_e32 v114, v186, v160
	v_exp_f32_e32 v220, v114
	v_add_f32_e32 v114, v186, v161
	v_exp_f32_e32 v222, v114
	v_add_f32_e32 v114, v186, v162
	v_exp_f32_e32 v217, v114
	v_add_f32_e32 v114, v186, v163
	v_exp_f32_e32 v219, v114
	v_add_f32_e32 v114, v186, v164
	v_exp_f32_e32 v221, v114
	v_add_f32_e32 v114, v186, v165
	v_exp_f32_e32 v223, v114
	v_add_f32_e32 v114, v186, v166
	v_exp_f32_e32 v224, v114
	v_add_f32_e32 v114, v186, v167
	v_exp_f32_e32 v226, v114
	v_add_f32_e32 v114, v186, v168
	v_exp_f32_e32 v228, v114
	v_add_f32_e32 v114, v186, v169
	v_exp_f32_e32 v230, v114
	v_add_f32_e32 v114, v186, v138
	v_exp_f32_e32 v225, v114
	v_add_f32_e32 v114, v186, v139
	v_exp_f32_e32 v227, v114
	v_add_f32_e32 v114, v186, v140
	v_exp_f32_e32 v229, v114
	v_add_f32_e32 v114, v186, v141
	v_exp_f32_e32 v231, v114
	v_add_f32_e32 v114, v186, v134
	v_exp_f32_e32 v232, v114
	v_add_f32_e32 v114, v186, v135
	v_exp_f32_e32 v234, v114
	v_add_f32_e32 v114, v186, v136
	v_exp_f32_e32 v236, v114
	v_add_f32_e32 v114, v186, v137
	v_exp_f32_e32 v238, v114
	v_add_f32_e32 v114, v186, v130
	v_exp_f32_e32 v233, v114
	v_add_f32_e32 v114, v186, v131
	v_exp_f32_e32 v235, v114
	v_add_f32_e32 v114, v186, v132
	v_exp_f32_e32 v237, v114
	v_add_f32_e32 v114, v186, v133
	v_exp_f32_e32 v239, v114
	v_cvt_pk_bf16_f32 v122, v152, v174
	v_cvt_pk_bf16_f32 v123, v190, v192
	v_cvt_pk_bf16_f32 v124, v216, v218
	v_cvt_pk_bf16_f32 v125, v220, v222
	v_cvt_pk_bf16_f32 v126, v153, v175
	v_cvt_pk_bf16_f32 v127, v191, v193
	v_cvt_pk_bf16_f32 v128, v217, v219
	v_cvt_pk_bf16_f32 v129, v221, v223
	v_cvt_pk_bf16_f32 v130, v224, v226
	v_cvt_pk_bf16_f32 v131, v228, v230
	v_cvt_pk_bf16_f32 v132, v232, v234
	v_cvt_pk_bf16_f32 v133, v236, v238
	v_cvt_pk_bf16_f32 v134, v225, v227
	v_cvt_pk_bf16_f32 v135, v229, v231
	v_cvt_pk_bf16_f32 v136, v233, v235
	v_cvt_pk_bf16_f32 v137, v237, v239
	s_waitcnt lgkmcnt(0)
	s_barrier
	ds_read_b128 v[114:117], v182 offset:33280
	ds_read_b128 v[118:121], v182 offset:33344
	ds_read_b128 v[144:147], v182 offset:37632
	ds_read_b128 v[148:151], v182 offset:37696
	ds_read_b128 v[162:165], v182 offset:41984
	ds_read_b128 v[166:169], v182 offset:42048
	ds_read_b128 v[196:199], v182 offset:46336
	ds_read_b128 v[200:203], v182 offset:46400
	s_waitcnt lgkmcnt(7)
	v_mfma_f32_16x16x32_bf16 v[138:141], v[114:117], v[22:25], 0
	v_mfma_f32_16x16x32_bf16 v[114:117], v[114:117], v[30:33], 0
	s_waitcnt lgkmcnt(5)
	v_mfma_f32_16x16x32_bf16 v[158:161], v[144:147], v[22:25], 0
	v_mfma_f32_16x16x32_bf16 v[144:147], v[144:147], v[30:33], 0
	s_waitcnt lgkmcnt(3)
	v_mfma_f32_16x16x32_bf16 v[170:173], v[162:165], v[22:25], 0
	v_mfma_f32_16x16x32_bf16 v[162:165], v[162:165], v[30:33], 0
	s_waitcnt lgkmcnt(1)
	v_mfma_f32_16x16x32_bf16 v[204:207], v[196:199], v[22:25], 0
	v_mfma_f32_16x16x32_bf16 v[196:199], v[196:199], v[30:33], 0
	v_mfma_f32_16x16x32_bf16 v[138:141], v[118:121], v[18:21], v[138:141]
	v_mfma_f32_16x16x32_bf16 v[114:117], v[118:121], v[26:29], v[114:117]
	v_mfma_f32_16x16x32_bf16 v[118:121], v[148:151], v[18:21], v[158:161]
	v_mfma_f32_16x16x32_bf16 v[144:147], v[148:151], v[26:29], v[144:147]
	v_mfma_f32_16x16x32_bf16 v[148:151], v[166:169], v[18:21], v[170:173]
	v_mfma_f32_16x16x32_bf16 v[158:161], v[166:169], v[26:29], v[162:165]
	s_waitcnt lgkmcnt(0)
	v_mfma_f32_16x16x32_bf16 v[166:169], v[200:203], v[26:29], v[196:199]
	ds_read_b128 v[170:173], v182 offset:33408
	s_nop 1
	ds_read_b128 v[196:199], v182 offset:33472
	v_mfma_f32_16x16x32_bf16 v[162:165], v[200:203], v[18:21], v[204:207]
	s_waitcnt lgkmcnt(1)
	v_mfma_f32_16x16x32_bf16 v[138:141], v[170:173], v[10:13], v[138:141]
	v_mfma_f32_16x16x32_bf16 v[114:117], v[170:173], v[14:17], v[114:117]
	ds_read_b128 v[170:173], v182 offset:37760
	ds_read_b128 v[200:203], v182 offset:37824
	s_waitcnt lgkmcnt(1)
	v_mfma_f32_16x16x32_bf16 v[118:121], v[170:173], v[10:13], v[118:121]
	v_mfma_f32_16x16x32_bf16 v[144:147], v[170:173], v[14:17], v[144:147]
	ds_read_b128 v[170:173], v182 offset:42112
	ds_read_b128 v[204:207], v182 offset:42176
	s_waitcnt lgkmcnt(1)
	v_mfma_f32_16x16x32_bf16 v[148:151], v[170:173], v[10:13], v[148:151]
	v_mfma_f32_16x16x32_bf16 v[158:161], v[170:173], v[14:17], v[158:161]
	ds_read_b128 v[170:173], v182 offset:46464
	ds_read_b128 v[208:211], v182 offset:46528
	s_waitcnt lgkmcnt(1)
; template <int D0> __device__ __forceinline__ void pv16(f32x4a (&o)[8][2], int vb, const bf16x8 (&pb)[2][2]) {
;     ...
;   const s16x4 a0 = TR(D0, 0, 0), a1 = TR(D0, 0, 1), a2 = TR(D0, 1, 0), a3 = TR(D0, 1, 1), b0 = TR(D0 + 1, 0, 0), b1 = TR(D0 + 1, 0, 1), b2 = TR(D0 + 1, 1, 0), b3 = TR(D0 + 1, 1, 1);
;   const s16x4 c0 = TR(D0 + 2, 0, 0), c1 = TR(D0 + 2, 0, 1), c2 = TR(D0 + 2, 1, 0), c3 = TR(D0 + 2, 1, 1);
;   asm volatile("s_waitcnt lgkmcnt(4)" ::: "memory"); SBAR();
;   o[D0][0] = MFMA16(PK16(a0, a1), pb[0][0], o[D0][0]); o[D0][1] = MFMA16(PK16(a0, a1), pb[0][1], o[D0][1]);
;   o[D0 + 1][0] = MFMA16(PK16(b0, b1), pb[0][0], o[D0 + 1][0]); o[D0 + 1][1] = MFMA16(PK16(b0, b1), pb[0][1], o[D0 + 1][1]);
;   o[D0][0] = MFMA16(PK16(a2, a3), pb[1][0], o[D0][0]); o[D0][1] = MFMA16(PK16(a2, a3), pb[1][1], o[D0][1]);
;   o[D0 + 1][0] = MFMA16(PK16(b2, b3), pb[1][0], o[D0 + 1][0]); o[D0 + 1][1] = MFMA16(PK16(b2, b3), pb[1][1], o[D0 + 1][1]);
;   SBAR();
;   const s16x4 d0 = TR(D0 + 3, 0, 0), d1 = TR(D0 + 3, 0, 1), d2 = TR(D0 + 3, 1, 0), d3 = TR(D0 + 3, 1, 1);
;   asm volatile("s_waitcnt lgkmcnt(4)" ::: "memory"); SBAR();
;   o[D0 + 2][0] = MFMA16(PK16(c0, c1), pb[0][0], o[D0 + 2][0]); o[D0 + 2][1] = MFMA16(PK16(c0, c1), pb[0][1], o[D0 + 2][1]);
;   o[D0 + 2][0] = MFMA16(PK16(c2, c3), pb[1][0], o[D0 + 2][0]); o[D0 + 2][1] = MFMA16(PK16(c2, c3), pb[1][1], o[D0 + 2][1]);
;   asm volatile("s_waitcnt lgkmcnt(0)" ::: "memory"); SBAR();
;   o[D0 + 3][0] = MFMA16(PK16(d0, d1), pb[0][0], o[D0 + 3][0]); o[D0 + 3][1] = MFMA16(PK16(d0, d1), pb[0][1], o[D0 + 3][1]);
;   o[D0 + 3][0] = MFMA16(PK16(d2, d3), pb[1][0], o[D0 + 3][0]); o[D0 + 3][1] = MFMA16(PK16(d2, d3), pb[1][1], o[D0 + 3][1]);
; template <int LDQ, int LDK, int LDO>
; __device__ __forceinline__ void attn_gqa16_body(const bf16* __restrict__ Qb, const bf16* __restrict__ Kh, const bf16* __restrict__ Vh, bf16* __restrict__ Ob, int seq, char* lds, float mref) {
;     ...
;   for (int t = 0; t < NT; ++t) {
;     HPACK();
;     __syncthreads();
;     const bool more = t + 1 < NT;
;     if (more) HQK((t + 1) & 1);
;     const int vb = vb0 + (t & 1) * (int)G16_V;
;     SBAR(); pv16<0>(o, vb, pb); SBAR();
;     asm volatile("s_waitcnt vmcnt(0)" ::: "memory");
;     if (t + 2 < NT) HWRITEK(t & 1);
;     if (t + 1 < NT) HWRITEV((t + 1) & 1);
;     HLOADK(t + 3); HLOADV(t + 2);
;     SBAR(); pv16<4>(o, vb, pb); SBAR();
	v_mfma_f32_16x16x32_bf16 v[162:165], v[170:173], v[10:13], v[162:165]
	v_mfma_f32_16x16x32_bf16 v[166:169], v[170:173], v[14:17], v[166:169]
	v_mfma_f32_16x16x32_bf16 v[170:173], v[196:199], v[2:5], v[138:141]
	v_mfma_f32_16x16x32_bf16 v[196:199], v[196:199], v[6:9], v[114:117]
	s_nop 1
	v_add_f32_e64 v138, v236, v238
	v_add_f32_e64 v139, v237, v239
	v_pk_add_f32 v[114:115], v[152:153], v[174:175]
	v_pk_add_f32 v[116:117], v[190:191], v[192:193]
	v_mfma_f32_16x16x32_bf16 v[212:215], v[200:203], v[2:5], v[118:121]
	v_add_f32_e64 v114, v114, v116
	v_add_f32_e64 v115, v115, v117
	v_pk_add_f32 v[116:117], v[216:217], v[218:219]
	v_pk_add_f32 v[114:115], v[142:143], v[114:115]
	v_pk_add_f32 v[118:119], v[220:221], v[222:223]
	v_pk_add_f32 v[120:121], v[228:229], v[230:231]
	v_pk_add_f32 v[116:117], v[116:117], v[118:119]
	v_pk_add_f32 v[118:119], v[224:225], v[226:227]
	v_pk_add_f32 v[114:115], v[116:117], v[114:115]
	v_pk_add_f32 v[118:119], v[118:119], v[120:121]
	v_pk_add_f32 v[120:121], v[232:233], v[234:235]
	v_pk_add_f32 v[114:115], v[118:119], v[114:115]
	v_pk_add_f32 v[120:121], v[120:121], v[138:139]
	v_mfma_f32_16x16x32_bf16 v[200:203], v[200:203], v[6:9], v[144:147]
	v_mfma_f32_16x16x32_bf16 v[150:153], v[204:207], v[2:5], v[148:151]
	v_mfma_f32_16x16x32_bf16 v[146:149], v[204:207], v[6:9], v[158:161]
	s_waitcnt lgkmcnt(0)
	v_mfma_f32_16x16x32_bf16 v[142:145], v[208:211], v[2:5], v[162:165]
	s_nop 0
	v_add_f32_e64 v158, v120, v114
	v_add_f32_e64 v159, v121, v115
	v_mfma_f32_16x16x32_bf16 v[138:141], v[208:211], v[6:9], v[166:169]
	ds_read_b64_tr_b16 v[114:115], v184 offset:0
	ds_read_b64_tr_b16 v[116:117], v184 offset:0x200
	ds_read_b64_tr_b16 v[118:119], v184 offset:0x400
	ds_read_b64_tr_b16 v[120:121], v184 offset:0x600
	ds_read_b64_tr_b16 v[160:161], v184 offset:0x820
	ds_read_b64_tr_b16 v[162:163], v184 offset:0xa20
	ds_read_b64_tr_b16 v[164:165], v184 offset:0xc20
	ds_read_b64_tr_b16 v[166:167], v184 offset:0xe20
	ds_read_b64_tr_b16 v[204:205], v184 offset:0x1040
	ds_read_b64_tr_b16 v[206:207], v184 offset:0x1240
	ds_read_b64_tr_b16 v[208:209], v184 offset:0x1440
	ds_read_b64_tr_b16 v[210:211], v184 offset:0x1640
	s_waitcnt lgkmcnt(4)
	s_nop 0
	v_mfma_f32_16x16x32_bf16 v[66:69], v[114:117], v[122:125], v[66:69]
	v_mfma_f32_16x16x32_bf16 v[114:117], v[114:117], v[126:129], v[70:73]
	v_mfma_f32_16x16x32_bf16 v[216:219], v[160:163], v[122:125], v[74:77]
	v_mfma_f32_16x16x32_bf16 v[160:163], v[160:163], v[126:129], v[78:81]
	v_mfma_f32_16x16x32_bf16 v[70:73], v[118:121], v[130:133], v[66:69]
	v_mfma_f32_16x16x32_bf16 v[74:77], v[118:121], v[134:137], v[114:117]
	v_mfma_f32_16x16x32_bf16 v[78:81], v[164:167], v[130:133], v[216:219]
	v_mfma_f32_16x16x32_bf16 v[114:117], v[164:167], v[134:137], v[160:163]
	ds_read_b64_tr_b16 v[66:67], v184 offset:0x1860
	ds_read_b64_tr_b16 v[68:69], v184 offset:0x1a60
	ds_read_b64_tr_b16 v[118:119], v184 offset:0x1c60
	ds_read_b64_tr_b16 v[120:121], v184 offset:0x1e60
	s_waitcnt lgkmcnt(4)
	v_mfma_f32_16x16x32_bf16 v[46:49], v[204:207], v[122:125], v[46:49]
	s_waitcnt lgkmcnt(0)
	v_mfma_f32_16x16x32_bf16 v[62:65], v[204:207], v[126:129], v[62:65]
	v_mfma_f32_16x16x32_bf16 v[46:49], v[208:211], v[130:133], v[46:49]
	v_mfma_f32_16x16x32_bf16 v[62:65], v[208:211], v[134:137], v[62:65]
	v_mfma_f32_16x16x32_bf16 v[50:53], v[66:69], v[122:125], v[50:53]
	v_mfma_f32_16x16x32_bf16 v[54:57], v[66:69], v[126:129], v[54:57]
	v_mfma_f32_16x16x32_bf16 v[50:53], v[118:121], v[130:133], v[50:53]
	v_mfma_f32_16x16x32_bf16 v[54:57], v[118:121], v[134:137], v[54:57]
	v_add_co_u32_e32 v66, vcc, s34, v156
	s_waitcnt vmcnt(0)
	s_nop 1
	v_addc_co_u32_e32 v67, vcc, 0, v157, vcc
	v_add_co_u32_e32 v118, vcc, s36, v156
	s_nop 1
	v_addc_co_u32_e32 v119, vcc, 0, v157, vcc
	global_load_dwordx4 v[66:69], v[66:67], off
	s_nop 0
	global_load_dwordx4 v[118:121], v[118:119], off
	s_waitcnt vmcnt(5)
	ds_write_b128 v194, v[34:37] offset:50688
	s_waitcnt vmcnt(4)
	ds_write_b128 v194, v[38:41] offset:59392
	s_waitcnt vmcnt(3)
	ds_write_b128 v181, v[42:45]
	s_waitcnt vmcnt(2)
	ds_write_b128 v181, v[58:61] offset:1024
	ds_read_b64_tr_b16 v[34:35], v184 offset:0x2080
	ds_read_b64_tr_b16 v[36:37], v184 offset:0x2280
	ds_read_b64_tr_b16 v[38:39], v184 offset:0x2480
	ds_read_b64_tr_b16 v[40:41], v184 offset:0x2680
	ds_read_b64_tr_b16 v[42:43], v184 offset:0x28a0
	ds_read_b64_tr_b16 v[44:45], v184 offset:0x2aa0
	ds_read_b64_tr_b16 v[58:59], v184 offset:0x2ca0
	ds_read_b64_tr_b16 v[60:61], v184 offset:0x2ea0
	ds_read_b64_tr_b16 v[160:161], v184 offset:0x30c0
	ds_read_b64_tr_b16 v[162:163], v184 offset:0x32c0
	ds_read_b64_tr_b16 v[164:165], v184 offset:0x34c0
	ds_read_b64_tr_b16 v[166:167], v184 offset:0x36c0
	s_waitcnt lgkmcnt(4)
	s_nop 0
	v_mfma_f32_16x16x32_bf16 v[98:101], v[34:37], v[122:125], v[98:101]
	v_mfma_f32_16x16x32_bf16 v[34:37], v[34:37], v[126:129], v[102:105]
	v_mfma_f32_16x16x32_bf16 v[106:109], v[42:45], v[122:125], v[106:109]
	v_mfma_f32_16x16x32_bf16 v[42:45], v[42:45], v[126:129], v[110:113]
	v_mfma_f32_16x16x32_bf16 v[98:101], v[38:41], v[130:133], v[98:101]
	v_mfma_f32_16x16x32_bf16 v[102:105], v[38:41], v[134:137], v[34:37]
	v_mfma_f32_16x16x32_bf16 v[106:109], v[58:61], v[130:133], v[106:109]
	v_mfma_f32_16x16x32_bf16 v[110:113], v[58:61], v[134:137], v[42:45]
	ds_read_b64_tr_b16 v[38:39], v184 offset:0x38e0
	ds_read_b64_tr_b16 v[40:41], v184 offset:0x3ae0
	ds_read_b64_tr_b16 v[42:43], v184 offset:0x3ce0
	ds_read_b64_tr_b16 v[44:45], v184 offset:0x3ee0
	s_waitcnt lgkmcnt(4)
	v_mfma_f32_16x16x32_bf16 v[34:37], v[160:163], v[122:125], v[82:85]
	s_waitcnt lgkmcnt(0)
; #define SBAR() __builtin_amdgcn_sched_barrier(0)
; #define HLOADV(kt) do { const char* vb_ = (const char*)Vh + (size_t)(kt) * (64 * LDK * 2); sv0 = *(const bf16x8*)(vb_ + koff0); sv1 = *(const bf16x8*)(vb_ + koff1); } while (0)
; #define HLOADK(kt) do { const char* kb_ = (const char*)Kh + (size_t)(kt) * (64 * LDK * 2); sk0 = *(const bf16x8*)(kb_ + koff0); sk1 = *(const bf16x8*)(kb_ + koff1); } while (0)
; #define HWRITEV(b) do { char* d_ = V_lds + (b) * G16_V; *(bf16x8*)(d_ + vst0) = sv0; *(bf16x8*)(d_ + vst1) = sv1; } while (0)
; #define HWRITEK(b) do { char* d_ = K_lds + (b) * GB_K; *(bf16x8*)(d_ + KSWZ(sr, sc * 2)) = sk0; *(bf16x8*)(d_ + KSWZ(32 + sr, sc * 2)) = sk1; } while (0)
; #define HEXP() do { _Pragma("unroll") for (int kt = 0; kt < 4; ++kt) { _Pragma("unroll") for (int qt = 0; qt < 2; ++qt) { _Pragma("unroll") for (int i = 0; i < 4; ++i) s[kt][qt][i] = __builtin_amdgcn_exp2f(fmaf(s[kt][qt][i], C, mnC)); } } } while (0)
; template <int LDQ, int LDK, int LDO>
; __device__ __forceinline__ void attn_gqa16_body(const bf16* __restrict__ Qb, const bf16* __restrict__ Kh, const bf16* __restrict__ Vh, bf16* __restrict__ Ob, int seq, char* lds, float mref) {
;     ...
;   const int NT = seq / KVBLK;
;   HLOADK(0); HLOADV(0); asm volatile("s_waitcnt vmcnt(0)" ::: "memory"); HWRITEK(0); HWRITEV(0);
;   HLOADK(1); asm volatile("s_waitcnt vmcnt(0)" ::: "memory"); HWRITEK(1); __syncthreads();
;   HLOADK(2); HLOADV(1);
;   HQK(0); HEXP();
;   if (wid >= 4) __builtin_amdgcn_s_setprio(1);
;   for (int t = 0; t < NT; ++t) {
;     HPACK();
;     __syncthreads();
;     const bool more = t + 1 < NT;
;     if (more) HQK((t + 1) & 1);
;     const int vb = vb0 + (t & 1) * (int)G16_V;
;     SBAR(); pv16<0>(o, vb, pb); SBAR();
	v_mfma_f32_16x16x32_bf16 v[58:61], v[160:163], v[126:129], v[94:97]
	v_mfma_f32_16x16x32_bf16 v[34:37], v[164:167], v[130:133], v[34:37]
	v_mfma_f32_16x16x32_bf16 v[58:61], v[164:167], v[134:137], v[58:61]
	v_mfma_f32_16x16x32_bf16 v[82:85], v[38:41], v[122:125], v[86:89]
	v_mfma_f32_16x16x32_bf16 v[86:89], v[38:41], v[126:129], v[90:93]
	v_mfma_f32_16x16x32_bf16 v[38:41], v[42:45], v[130:133], v[82:85]
	v_mfma_f32_16x16x32_bf16 v[42:45], v[42:45], v[134:137], v[86:89]
	s_nop 4
	v_add_f32_e32 v82, v186, v170
	v_exp_f32_e32 v157, v82
	v_add_f32_e32 v82, v186, v171
	v_exp_f32_e32 v191, v82
	v_add_f32_e32 v82, v186, v172
	v_exp_f32_e32 v193, v82
	v_add_f32_e32 v82, v186, v173
	v_exp_f32_e32 v205, v82
	v_add_f32_e32 v82, v186, v196
	v_exp_f32_e32 v207, v82
	v_add_f32_e32 v82, v186, v197
	v_exp_f32_e32 v197, v82
	v_add_f32_e32 v82, v186, v198
	v_exp_f32_e32 v209, v82
	v_add_f32_e32 v82, v186, v199
	v_exp_f32_e32 v199, v82
	v_add_f32_e32 v82, v186, v212
	v_exp_f32_e32 v156, v82
	v_add_f32_e32 v82, v186, v213
	v_exp_f32_e32 v190, v82
	v_add_f32_e32 v82, v186, v214
	v_exp_f32_e32 v192, v82
	v_add_f32_e32 v82, v186, v215
	v_exp_f32_e32 v204, v82
	v_add_f32_e32 v82, v186, v200
	v_exp_f32_e32 v206, v82
	v_add_f32_e32 v82, v186, v201
	v_exp_f32_e32 v196, v82
	v_add_f32_e32 v82, v186, v202
	v_exp_f32_e32 v208, v82
	v_add_f32_e32 v82, v186, v203
	v_exp_f32_e32 v198, v82
	v_add_f32_e32 v82, v186, v150
	v_exp_f32_e32 v200, v82
	v_add_f32_e32 v82, v186, v151
	v_exp_f32_e32 v202, v82
	v_add_f32_e32 v82, v186, v152
	v_exp_f32_e32 v201, v82
	v_add_f32_e32 v82, v186, v153
	v_exp_f32_e32 v203, v82
	v_add_f32_e32 v82, v186, v146
	v_exp_f32_e32 v210, v82
	v_add_f32_e32 v82, v186, v147
	v_exp_f32_e32 v212, v82
	v_add_f32_e32 v82, v186, v148
	v_exp_f32_e32 v211, v82
	v_add_f32_e32 v82, v186, v149
	v_exp_f32_e32 v213, v82
	v_add_f32_e32 v82, v186, v142
	v_exp_f32_e32 v189, v82
	v_add_f32_e32 v82, v186, v143
	v_exp_f32_e32 v195, v82
	v_add_f32_e32 v82, v186, v144
	v_exp_f32_e32 v214, v82
	v_add_f32_e32 v82, v186, v145
	v_exp_f32_e32 v215, v82
	v_add_f32_e32 v82, v186, v138
	v_exp_f32_e32 v216, v82
	v_add_f32_e32 v82, v186, v139
	v_exp_f32_e32 v217, v82
	v_add_f32_e32 v82, v186, v140
	v_exp_f32_e32 v218, v82
	v_add_f32_e32 v82, v186, v141
	v_exp_f32_e32 v219, v82
	v_cvt_pk_bf16_f32 v82, v157, v191
	v_cvt_pk_bf16_f32 v83, v193, v205
	v_cvt_pk_bf16_f32 v84, v156, v190
	v_cvt_pk_bf16_f32 v85, v192, v204
	v_cvt_pk_bf16_f32 v86, v207, v197
	v_cvt_pk_bf16_f32 v87, v209, v199
	v_cvt_pk_bf16_f32 v88, v206, v196
	v_cvt_pk_bf16_f32 v89, v208, v198
	v_cvt_pk_bf16_f32 v90, v200, v202
	v_cvt_pk_bf16_f32 v91, v201, v203
	v_cvt_pk_bf16_f32 v92, v189, v195
	v_cvt_pk_bf16_f32 v93, v214, v215
	v_cvt_pk_bf16_f32 v94, v210, v212
	v_cvt_pk_bf16_f32 v95, v211, v213
	v_cvt_pk_bf16_f32 v96, v216, v217
	v_cvt_pk_bf16_f32 v97, v218, v219
	s_waitcnt lgkmcnt(0)
	s_barrier
	ds_read_b128 v[122:125], v182 offset:50688
	ds_read_b128 v[126:129], v182 offset:50752
	ds_read_b128 v[134:137], v182 offset:55040
	ds_read_b128 v[138:141], v182 offset:55104
	ds_read_b128 v[146:149], v182 offset:59392
	ds_read_b128 v[150:153], v182 offset:59456
	ds_read_b128 v[164:167], v182 offset:63744
	ds_read_b128 v[168:171], v182 offset:63808
	s_waitcnt lgkmcnt(7)
	v_mfma_f32_16x16x32_bf16 v[130:133], v[122:125], v[22:25], 0
	v_mfma_f32_16x16x32_bf16 v[122:125], v[122:125], v[30:33], 0
	s_waitcnt lgkmcnt(5)
	v_mfma_f32_16x16x32_bf16 v[142:145], v[134:137], v[22:25], 0
	v_mfma_f32_16x16x32_bf16 v[134:137], v[134:137], v[30:33], 0
	s_waitcnt lgkmcnt(3)
	v_mfma_f32_16x16x32_bf16 v[160:163], v[146:149], v[22:25], 0
	v_mfma_f32_16x16x32_bf16 v[146:149], v[146:149], v[30:33], 0
	s_waitcnt lgkmcnt(1)
	v_mfma_f32_16x16x32_bf16 v[22:25], v[164:167], v[22:25], 0
	v_mfma_f32_16x16x32_bf16 v[30:33], v[164:167], v[30:33], 0
	v_mfma_f32_16x16x32_bf16 v[130:133], v[126:129], v[18:21], v[130:133]
	v_mfma_f32_16x16x32_bf16 v[122:125], v[126:129], v[26:29], v[122:125]
	v_mfma_f32_16x16x32_bf16 v[126:129], v[138:141], v[18:21], v[142:145]
	v_mfma_f32_16x16x32_bf16 v[134:137], v[138:141], v[26:29], v[134:137]
	v_mfma_f32_16x16x32_bf16 v[138:141], v[150:153], v[18:21], v[160:163]
	v_mfma_f32_16x16x32_bf16 v[142:145], v[150:153], v[26:29], v[146:149]
	s_waitcnt lgkmcnt(0)
	v_mfma_f32_16x16x32_bf16 v[18:21], v[168:171], v[18:21], v[22:25]
	v_mfma_f32_16x16x32_bf16 v[22:25], v[168:171], v[26:29], v[30:33]
	ds_read_b128 v[26:29], v182 offset:50816
	s_nop 1
	ds_read_b128 v[30:33], v182 offset:50880
	s_waitcnt lgkmcnt(1)
	v_mfma_f32_16x16x32_bf16 v[130:133], v[26:29], v[10:13], v[130:133]
	v_mfma_f32_16x16x32_bf16 v[26:29], v[26:29], v[14:17], v[122:125]
	s_nop 2
	ds_read_b128 v[122:125], v182 offset:55168
	ds_read_b128 v[146:149], v182 offset:55232
	s_waitcnt lgkmcnt(1)
	v_mfma_f32_16x16x32_bf16 v[126:129], v[122:125], v[10:13], v[126:129]
	v_mfma_f32_16x16x32_bf16 v[122:125], v[122:125], v[14:17], v[134:137]
	s_nop 2
	ds_read_b128 v[134:137], v182 offset:59520
	ds_read_b128 v[150:153], v182 offset:59584
	s_waitcnt lgkmcnt(1)
	v_mfma_f32_16x16x32_bf16 v[138:141], v[134:137], v[10:13], v[138:141]
	v_mfma_f32_16x16x32_bf16 v[142:145], v[134:137], v[14:17], v[142:145]
	ds_read_b128 v[134:137], v182 offset:63872
	ds_read_b128 v[160:163], v182 offset:63936
	s_waitcnt lgkmcnt(1)
; template <int D0> __device__ __forceinline__ void pv16(f32x4a (&o)[8][2], int vb, const bf16x8 (&pb)[2][2]) {
;     ...
;   const s16x4 a0 = TR(D0, 0, 0), a1 = TR(D0, 0, 1), a2 = TR(D0, 1, 0), a3 = TR(D0, 1, 1), b0 = TR(D0 + 1, 0, 0), b1 = TR(D0 + 1, 0, 1), b2 = TR(D0 + 1, 1, 0), b3 = TR(D0 + 1, 1, 1);
;   const s16x4 c0 = TR(D0 + 2, 0, 0), c1 = TR(D0 + 2, 0, 1), c2 = TR(D0 + 2, 1, 0), c3 = TR(D0 + 2, 1, 1);
;   asm volatile("s_waitcnt lgkmcnt(4)" ::: "memory"); SBAR();
;   o[D0][0] = MFMA16(PK16(a0, a1), pb[0][0], o[D0][0]); o[D0][1] = MFMA16(PK16(a0, a1), pb[0][1], o[D0][1]);
;   o[D0 + 1][0] = MFMA16(PK16(b0, b1), pb[0][0], o[D0 + 1][0]); o[D0 + 1][1] = MFMA16(PK16(b0, b1), pb[0][1], o[D0 + 1][1]);
;   o[D0][0] = MFMA16(PK16(a2, a3), pb[1][0], o[D0][0]); o[D0][1] = MFMA16(PK16(a2, a3), pb[1][1], o[D0][1]);
;   o[D0 + 1][0] = MFMA16(PK16(b2, b3), pb[1][0], o[D0 + 1][0]); o[D0 + 1][1] = MFMA16(PK16(b2, b3), pb[1][1], o[D0 + 1][1]);
;   SBAR();
;   const s16x4 d0 = TR(D0 + 3, 0, 0), d1 = TR(D0 + 3, 0, 1), d2 = TR(D0 + 3, 1, 0), d3 = TR(D0 + 3, 1, 1);
;   asm volatile("s_waitcnt lgkmcnt(4)" ::: "memory"); SBAR();
;   o[D0 + 2][0] = MFMA16(PK16(c0, c1), pb[0][0], o[D0 + 2][0]); o[D0 + 2][1] = MFMA16(PK16(c0, c1), pb[0][1], o[D0 + 2][1]);
;   o[D0 + 2][0] = MFMA16(PK16(c2, c3), pb[1][0], o[D0 + 2][0]); o[D0 + 2][1] = MFMA16(PK16(c2, c3), pb[1][1], o[D0 + 2][1]);
;   asm volatile("s_waitcnt lgkmcnt(0)" ::: "memory"); SBAR();
;   o[D0 + 3][0] = MFMA16(PK16(d0, d1), pb[0][0], o[D0 + 3][0]); o[D0 + 3][1] = MFMA16(PK16(d0, d1), pb[0][1], o[D0 + 3][1]);
;   o[D0 + 3][0] = MFMA16(PK16(d2, d3), pb[1][0], o[D0 + 3][0]); o[D0 + 3][1] = MFMA16(PK16(d2, d3), pb[1][1], o[D0 + 3][1]);
; template <int LDQ, int LDK, int LDO>
; __device__ __forceinline__ void attn_gqa16_body(const bf16* __restrict__ Qb, const bf16* __restrict__ Kh, const bf16* __restrict__ Vh, bf16* __restrict__ Ob, int seq, char* lds, float mref) {
;     ...
;   for (int t = 0; t < NT; ++t) {
;     HPACK();
;     __syncthreads();
;     const bool more = t + 1 < NT;
;     if (more) HQK((t + 1) & 1);
;     const int vb = vb0 + (t & 1) * (int)G16_V;
;     SBAR(); pv16<0>(o, vb, pb); SBAR();
;     asm volatile("s_waitcnt vmcnt(0)" ::: "memory");
;     if (t + 2 < NT) HWRITEK(t & 1);
;     if (t + 1 < NT) HWRITEV((t + 1) & 1);
;     HLOADK(t + 3); HLOADV(t + 2);
;     SBAR(); pv16<4>(o, vb, pb); SBAR();
	v_mfma_f32_16x16x32_bf16 v[10:13], v[134:137], v[10:13], v[18:21]
	s_nop 2
	v_add_f32_e64 v18, v156, v190
	v_add_f32_e64 v19, v157, v191
	v_mfma_f32_16x16x32_bf16 v[14:17], v[134:137], v[14:17], v[22:25]
	v_add_f32_e64 v20, v192, v204
	v_add_f32_e64 v21, v193, v205
	v_pk_add_f32 v[136:137], v[210:211], v[212:213]
	v_pk_add_f32 v[18:19], v[18:19], v[20:21]
	v_mfma_f32_16x16x32_bf16 v[164:167], v[30:33], v[2:5], v[130:133]
	v_add_f32_e64 v22, v206, v196
	v_add_f32_e64 v23, v207, v197
	v_pk_add_f32 v[24:25], v[208:209], v[198:199]
	v_mfma_f32_16x16x32_bf16 v[172:175], v[146:149], v[2:5], v[126:129]
	v_add_f32_e64 v134, v22, v24
	v_add_f32_e64 v135, v23, v25
	v_add_f32_e32 v130, v189, v195
	v_add_f32_e32 v132, v214, v215
	v_mfma_f32_16x16x32_bf16 v[138:141], v[150:153], v[2:5], v[138:141]
	v_add_f32_e64 v126, v200, v202
	v_add_f32_e64 v127, v201, v203
	v_mfma_f32_16x16x32_bf16 v[142:145], v[150:153], v[6:9], v[142:145]
	s_waitcnt lgkmcnt(0)
	v_mfma_f32_16x16x32_bf16 v[150:153], v[160:163], v[2:5], v[10:13]
	v_add_f32_e64 v2, v158, v19
	v_add_f32_e64 v3, v159, v18
	v_pk_add_f32 v[128:129], v[18:19], v[2:3]
	v_mfma_f32_16x16x32_bf16 v[168:171], v[30:33], v[6:9], v[26:29]
	v_mfma_f32_16x16x32_bf16 v[146:149], v[146:149], v[6:9], v[122:125]
	s_nop 2
	v_add_f32_e32 v122, v216, v217
	v_add_f32_e32 v124, v218, v219
	v_mfma_f32_16x16x32_bf16 v[160:163], v[160:163], v[6:9], v[14:17]
	ds_read_b64_tr_b16 v[2:3], v183 offset:0
	ds_read_b64_tr_b16 v[4:5], v183 offset:0x200
	ds_read_b64_tr_b16 v[6:7], v183 offset:0x400
	ds_read_b64_tr_b16 v[8:9], v183 offset:0x600
	ds_read_b64_tr_b16 v[10:11], v183 offset:0x820
	ds_read_b64_tr_b16 v[12:13], v183 offset:0xa20
	ds_read_b64_tr_b16 v[14:15], v183 offset:0xc20
	ds_read_b64_tr_b16 v[16:17], v183 offset:0xe20
	ds_read_b64_tr_b16 v[18:19], v183 offset:0x1040
	ds_read_b64_tr_b16 v[20:21], v183 offset:0x1240
	ds_read_b64_tr_b16 v[22:23], v183 offset:0x1440
	ds_read_b64_tr_b16 v[24:25], v183 offset:0x1640
	s_waitcnt lgkmcnt(4)
	s_nop 0
	v_mfma_f32_16x16x32_bf16 v[26:29], v[2:5], v[82:85], v[70:73]
	v_mfma_f32_16x16x32_bf16 v[30:33], v[2:5], v[86:89], v[74:77]
	v_mfma_f32_16x16x32_bf16 v[70:73], v[10:13], v[82:85], v[78:81]
	v_mfma_f32_16x16x32_bf16 v[10:13], v[10:13], v[86:89], v[114:117]
	v_mfma_f32_16x16x32_bf16 v[2:5], v[6:9], v[90:93], v[26:29]
	v_mfma_f32_16x16x32_bf16 v[6:9], v[6:9], v[94:97], v[30:33]
	v_mfma_f32_16x16x32_bf16 v[70:73], v[14:17], v[90:93], v[70:73]
	v_mfma_f32_16x16x32_bf16 v[74:77], v[14:17], v[94:97], v[10:13]
	ds_read_b64_tr_b16 v[14:15], v183 offset:0x1860
	ds_read_b64_tr_b16 v[16:17], v183 offset:0x1a60
	ds_read_b64_tr_b16 v[26:27], v183 offset:0x1c60
	ds_read_b64_tr_b16 v[28:29], v183 offset:0x1e60
	s_waitcnt lgkmcnt(4)
	v_mfma_f32_16x16x32_bf16 v[10:13], v[18:21], v[82:85], v[46:49]
	s_waitcnt lgkmcnt(0)
	v_mfma_f32_16x16x32_bf16 v[18:21], v[18:21], v[86:89], v[62:65]
	v_mfma_f32_16x16x32_bf16 v[10:13], v[22:25], v[90:93], v[10:13]
	v_mfma_f32_16x16x32_bf16 v[22:25], v[22:25], v[94:97], v[18:21]
	v_mfma_f32_16x16x32_bf16 v[18:21], v[14:17], v[82:85], v[50:53]
	v_mfma_f32_16x16x32_bf16 v[30:33], v[14:17], v[86:89], v[54:57]
	v_mfma_f32_16x16x32_bf16 v[14:17], v[26:29], v[90:93], v[18:21]
	v_mfma_f32_16x16x32_bf16 v[18:21], v[26:29], v[94:97], v[30:33]
	s_waitcnt vmcnt(0)
	s_waitcnt vmcnt(1)
	ds_write_b128 v181, v[66:69] offset:16640
	s_waitcnt vmcnt(0)
	ds_write_b128 v181, v[118:121] offset:17664
	ds_read_b64_tr_b16 v[26:27], v183 offset:0x2080
	ds_read_b64_tr_b16 v[28:29], v183 offset:0x2280
	ds_read_b64_tr_b16 v[30:31], v183 offset:0x2480
	ds_read_b64_tr_b16 v[32:33], v183 offset:0x2680
	ds_read_b64_tr_b16 v[46:47], v183 offset:0x28a0
	ds_read_b64_tr_b16 v[48:49], v183 offset:0x2aa0
	ds_read_b64_tr_b16 v[62:63], v183 offset:0x2ca0
	ds_read_b64_tr_b16 v[64:65], v183 offset:0x2ea0
	ds_read_b64_tr_b16 v[114:115], v183 offset:0x30c0
	ds_read_b64_tr_b16 v[116:117], v183 offset:0x32c0
	ds_read_b64_tr_b16 v[118:119], v183 offset:0x34c0
	ds_read_b64_tr_b16 v[120:121], v183 offset:0x36c0
	s_waitcnt lgkmcnt(4)
	s_nop 0
	v_mfma_f32_16x16x32_bf16 v[50:53], v[26:29], v[82:85], v[98:101]
	v_mfma_f32_16x16x32_bf16 v[26:29], v[26:29], v[86:89], v[102:105]
	v_mfma_f32_16x16x32_bf16 v[66:69], v[46:49], v[82:85], v[106:109]
	v_mfma_f32_16x16x32_bf16 v[46:49], v[46:49], v[86:89], v[110:113]
	v_mfma_f32_16x16x32_bf16 v[50:53], v[30:33], v[90:93], v[50:53]
	v_mfma_f32_16x16x32_bf16 v[54:57], v[30:33], v[94:97], v[26:29]
	v_mfma_f32_16x16x32_bf16 v[66:69], v[62:65], v[90:93], v[66:69]
	v_mfma_f32_16x16x32_bf16 v[78:81], v[62:65], v[94:97], v[46:49]
	ds_read_b64_tr_b16 v[30:31], v183 offset:0x38e0
	ds_read_b64_tr_b16 v[32:33], v183 offset:0x3ae0
	ds_read_b64_tr_b16 v[46:47], v183 offset:0x3ce0
	ds_read_b64_tr_b16 v[48:49], v183 offset:0x3ee0
	s_waitcnt lgkmcnt(4)
	v_mfma_f32_16x16x32_bf16 v[26:29], v[114:117], v[82:85], v[34:37]
	s_waitcnt lgkmcnt(0)
; template <int D0> __device__ __forceinline__ void pv16(f32x4a (&o)[8][2], int vb, const bf16x8 (&pb)[2][2]) {
;     ...
;   const s16x4 a0 = TR(D0, 0, 0), a1 = TR(D0, 0, 1), a2 = TR(D0, 1, 0), a3 = TR(D0, 1, 1), b0 = TR(D0 + 1, 0, 0), b1 = TR(D0 + 1, 0, 1), b2 = TR(D0 + 1, 1, 0), b3 = TR(D0 + 1, 1, 1);
;   const s16x4 c0 = TR(D0 + 2, 0, 0), c1 = TR(D0 + 2, 0, 1), c2 = TR(D0 + 2, 1, 0), c3 = TR(D0 + 2, 1, 1);
;   asm volatile("s_waitcnt lgkmcnt(4)" ::: "memory"); SBAR();
;   o[D0][0] = MFMA16(PK16(a0, a1), pb[0][0], o[D0][0]); o[D0][1] = MFMA16(PK16(a0, a1), pb[0][1], o[D0][1]);
;   o[D0 + 1][0] = MFMA16(PK16(b0, b1), pb[0][0], o[D0 + 1][0]); o[D0 + 1][1] = MFMA16(PK16(b0, b1), pb[0][1], o[D0 + 1][1]);
;   o[D0][0] = MFMA16(PK16(a2, a3), pb[1][0], o[D0][0]); o[D0][1] = MFMA16(PK16(a2, a3), pb[1][1], o[D0][1]);
;   o[D0 + 1][0] = MFMA16(PK16(b2, b3), pb[1][0], o[D0 + 1][0]); o[D0 + 1][1] = MFMA16(PK16(b2, b3), pb[1][1], o[D0 + 1][1]);
;   SBAR();
;   const s16x4 d0 = TR(D0 + 3, 0, 0), d1 = TR(D0 + 3, 0, 1), d2 = TR(D0 + 3, 1, 0), d3 = TR(D0 + 3, 1, 1);
;   asm volatile("s_waitcnt lgkmcnt(4)" ::: "memory"); SBAR();
;   o[D0 + 2][0] = MFMA16(PK16(c0, c1), pb[0][0], o[D0 + 2][0]); o[D0 + 2][1] = MFMA16(PK16(c0, c1), pb[0][1], o[D0 + 2][1]);
;   o[D0 + 2][0] = MFMA16(PK16(c2, c3), pb[1][0], o[D0 + 2][0]); o[D0 + 2][1] = MFMA16(PK16(c2, c3), pb[1][1], o[D0 + 2][1]);
;   asm volatile("s_waitcnt lgkmcnt(0)" ::: "memory"); SBAR();
;   o[D0 + 3][0] = MFMA16(PK16(d0, d1), pb[0][0], o[D0 + 3][0]); o[D0 + 3][1] = MFMA16(PK16(d0, d1), pb[0][1], o[D0 + 3][1]);
;   o[D0 + 3][0] = MFMA16(PK16(d2, d3), pb[1][0], o[D0 + 3][0]); o[D0 + 3][1] = MFMA16(PK16(d2, d3), pb[1][1], o[D0 + 3][1]);
; template <int LDQ, int LDK, int LDO>
; __device__ __forceinline__ void attn_gqa16_body(const bf16* __restrict__ Qb, const bf16* __restrict__ Kh, const bf16* __restrict__ Vh, bf16* __restrict__ Ob, int seq, char* lds, float mref) {
;     ...
;   const int NT = seq / KVBLK;
;   HLOADK(0); HLOADV(0); asm volatile("s_waitcnt vmcnt(0)" ::: "memory"); HWRITEK(0); HWRITEV(0);
;   HLOADK(1); asm volatile("s_waitcnt vmcnt(0)" ::: "memory"); HWRITEK(1); __syncthreads();
;   HLOADK(2); HLOADV(1);
;   HQK(0); HEXP();
;   if (wid >= 4) __builtin_amdgcn_s_setprio(1);
;   for (int t = 0; t < NT; ++t) {
;     HPACK();
;     __syncthreads();
;     const bool more = t + 1 < NT;
;     if (more) HQK((t + 1) & 1);
	v_mfma_f32_16x16x32_bf16 v[34:37], v[114:117], v[86:89], v[58:61]
	v_mfma_f32_16x16x32_bf16 v[26:29], v[118:121], v[90:93], v[26:29]
	v_mfma_f32_16x16x32_bf16 v[58:61], v[118:121], v[94:97], v[34:37]
	v_mfma_f32_16x16x32_bf16 v[34:37], v[30:33], v[82:85], v[38:41]
	v_mfma_f32_16x16x32_bf16 v[38:41], v[30:33], v[86:89], v[42:45]
	v_mfma_f32_16x16x32_bf16 v[30:33], v[46:49], v[90:93], v[34:37]
	v_mfma_f32_16x16x32_bf16 v[62:65], v[46:49], v[94:97], v[38:41]
	s_nop 5
	v_add_f32_e32 v38, v186, v138
	v_exp_f32_e32 v88, v38
	v_add_f32_e32 v38, v186, v139
	v_exp_f32_e32 v116, v38
	v_add_f32_e32 v38, v186, v140
	v_exp_f32_e32 v117, v38
	v_add_f32_e32 v38, v186, v141
	v_exp_f32_e32 v118, v38
	v_add_f32_e32 v38, v186, v142
	v_add_f32_e32 v34, v186, v164
	v_exp_f32_e32 v102, v38
	v_add_f32_e32 v38, v186, v143
	v_exp_f32_e32 v131, v34
	v_add_f32_e32 v34, v186, v165
	v_exp_f32_e32 v103, v38
	v_add_f32_e32 v38, v186, v144
	v_exp_f32_e32 v133, v34
	v_add_f32_e32 v34, v186, v166
	v_exp_f32_e32 v104, v38
	v_add_f32_e32 v38, v186, v145
	v_exp_f32_e32 v48, v34
	v_add_f32_e32 v34, v186, v167
	v_exp_f32_e32 v105, v38
	v_add_f32_e32 v38, v186, v150
	v_exp_f32_e32 v129, v34
	v_add_f32_e32 v34, v186, v168
	v_exp_f32_e32 v119, v38
	v_add_f32_e32 v38, v186, v151
	v_exp_f32_e32 v123, v34
	v_add_f32_e32 v34, v186, v169
	v_exp_f32_e32 v120, v38
	v_add_f32_e32 v38, v186, v152
	v_exp_f32_e32 v125, v34
	v_add_f32_e32 v34, v186, v170
	v_exp_f32_e32 v87, v38
	v_add_f32_e32 v38, v186, v153
	v_exp_f32_e32 v49, v34
	v_add_f32_e32 v34, v186, v171
	v_exp_f32_e32 v89, v38
	v_add_f32_e32 v38, v186, v160
	v_exp_f32_e32 v86, v34
	v_add_f32_e32 v34, v186, v172
	v_exp_f32_e32 v106, v38
	v_add_f32_e32 v38, v186, v161
	v_exp_f32_e32 v82, v34
	v_add_f32_e32 v34, v186, v173
	v_exp_f32_e32 v107, v38
	v_add_f32_e32 v38, v186, v162
	v_exp_f32_e32 v84, v34
	v_add_f32_e32 v34, v186, v174
	v_exp_f32_e32 v39, v38
	v_exp_f32_e32 v83, v34
	v_add_f32_e32 v34, v186, v175
	v_add_f32_e32 v35, v186, v147
	v_exp_f32_e32 v85, v34
	v_add_f32_e32 v34, v186, v146
	v_exp_f32_e32 v36, v35
	v_add_f32_e32 v35, v186, v148
	v_add_f32_e32 v37, v186, v149
	v_add_f32_e32 v38, v186, v163
	v_exp_f32_e32 v34, v34
	v_exp_f32_e32 v35, v35
	v_exp_f32_e32 v37, v37
	v_exp_f32_e32 v41, v38
	v_add_f32_e32 v38, v135, v159
	v_pk_add_f32 v[44:45], v[136:137], v[136:137] op_sel:[0,1] op_sel_hi:[1,0]
	v_pk_add_f32 v[46:47], v[134:135], v[38:39] op_sel_hi:[1,0]
	v_mov_b32_e32 v45, v49
	v_mov_b32_e32 v47, v86
	v_pk_add_f32 v[42:43], v[122:123], v[124:125]
	v_pk_add_f32 v[44:45], v[44:45], v[46:47]
	v_add_f32_e32 v38, v102, v103
	v_pk_add_f32 v[42:43], v[42:43], v[44:45]
	v_pk_add_f32 v[44:45], v[34:35], v[36:37]
	v_pk_add_f32 v[42:43], v[42:43], v[42:43] op_sel:[0,1] op_sel_hi:[1,0]
	v_pk_add_f32 v[44:45], v[44:45], v[44:45] op_sel:[0,1] op_sel_hi:[1,0]
	v_add_f32_e32 v40, v104, v105
	v_mov_b32_e32 v43, v106
	v_mov_b32_e32 v45, v107
	v_pk_add_f32 v[42:43], v[42:43], v[44:45]
	v_pk_add_f32 v[44:45], v[38:39], v[40:41]
	v_cvt_pk_bf16_f32 v90, v131, v133
	v_cvt_pk_bf16_f32 v91, v48, v129
	v_cvt_pk_bf16_f32 v92, v82, v84
	v_cvt_pk_bf16_f32 v93, v83, v85
	v_cvt_pk_bf16_f32 v94, v123, v125
	s_nop 0
	v_pk_add_f32 v[42:43], v[42:43], v[44:45]
	v_pk_add_f32 v[44:45], v[126:127], v[126:127] op_sel:[0,1] op_sel_hi:[1,0]
	v_add_f32_e32 v121, v42, v43
	v_mov_b32_e32 v45, v48
	v_pk_add_f32 v[42:43], v[130:131], v[132:133]
	v_pk_add_f32 v[44:45], v[44:45], v[128:129]
	v_cvt_pk_bf16_f32 v95, v49, v86
	v_cvt_pk_bf16_f32 v96, v34, v36
	v_cvt_pk_bf16_f32 v97, v35, v37
	v_cvt_pk_bf16_f32 v98, v88, v116
	v_cvt_pk_bf16_f32 v99, v117, v118
	s_nop 0
	v_pk_add_f32 v[114:115], v[42:43], v[44:45]
	v_cvt_pk_bf16_f32 v100, v119, v120
	v_cvt_pk_bf16_f32 v101, v87, v89
	v_cvt_pk_bf16_f32 v102, v102, v103
	v_cvt_pk_bf16_f32 v103, v104, v105
	v_cvt_pk_bf16_f32 v104, v106, v107
	v_cvt_pk_bf16_f32 v105, v39, v41
	s_waitcnt lgkmcnt(0)
	s_barrier
	ds_read_b64_tr_b16 v[34:35], v184 offset:0
	ds_read_b64_tr_b16 v[36:37], v184 offset:0x200
	ds_read_b64_tr_b16 v[42:43], v184 offset:0x400
	ds_read_b64_tr_b16 v[44:45], v184 offset:0x600
	ds_read_b64_tr_b16 v[38:39], v184 offset:0x820
	ds_read_b64_tr_b16 v[40:41], v184 offset:0xa20
	ds_read_b64_tr_b16 v[46:47], v184 offset:0xc20
	ds_read_b64_tr_b16 v[48:49], v184 offset:0xe20
	ds_read_b64_tr_b16 v[106:107], v184 offset:0x1040
	ds_read_b64_tr_b16 v[108:109], v184 offset:0x1240
	ds_read_b64_tr_b16 v[110:111], v184 offset:0x1440
	ds_read_b64_tr_b16 v[112:113], v184 offset:0x1640
	s_waitcnt lgkmcnt(4)
	s_nop 0
	v_mfma_f32_16x16x32_bf16 v[2:5], v[34:37], v[90:93], v[2:5]
	v_mfma_f32_16x16x32_bf16 v[6:9], v[34:37], v[94:97], v[6:9]
	v_mfma_f32_16x16x32_bf16 v[34:37], v[38:41], v[90:93], v[70:73]
	v_mfma_f32_16x16x32_bf16 v[70:73], v[38:41], v[94:97], v[74:77]
	v_mfma_f32_16x16x32_bf16 v[38:41], v[42:45], v[98:101], v[2:5]
	v_mfma_f32_16x16x32_bf16 v[6:9], v[42:45], v[102:105], v[6:9]
	v_mfma_f32_16x16x32_bf16 v[34:37], v[46:49], v[98:101], v[34:37]
	v_mfma_f32_16x16x32_bf16 v[2:5], v[46:49], v[102:105], v[70:73]
	ds_read_b64_tr_b16 v[46:47], v184 offset:0x1860
	ds_read_b64_tr_b16 v[48:49], v184 offset:0x1a60
	ds_read_b64_tr_b16 v[70:71], v184 offset:0x1c60
	ds_read_b64_tr_b16 v[72:73], v184 offset:0x1e60
	s_waitcnt lgkmcnt(4)
	v_mfma_f32_16x16x32_bf16 v[10:13], v[106:109], v[90:93], v[10:13]
	s_waitcnt lgkmcnt(0)
	v_mfma_f32_16x16x32_bf16 v[22:25], v[106:109], v[94:97], v[22:25]
	v_mfma_f32_16x16x32_bf16 v[42:45], v[110:113], v[98:101], v[10:13]
	v_mfma_f32_16x16x32_bf16 v[10:13], v[110:113], v[102:105], v[22:25]
	v_mfma_f32_16x16x32_bf16 v[14:17], v[46:49], v[90:93], v[14:17]
	v_mfma_f32_16x16x32_bf16 v[18:21], v[46:49], v[94:97], v[18:21]
	v_mfma_f32_16x16x32_bf16 v[46:49], v[70:73], v[98:101], v[14:17]
	v_mfma_f32_16x16x32_bf16 v[14:17], v[70:73], v[102:105], v[18:21]
	s_waitcnt vmcnt(0)
; #define SBAR() __builtin_amdgcn_sched_barrier(0)
; #define HLOADV(kt) do { const char* vb_ = (const char*)Vh + (size_t)(kt) * (64 * LDK * 2); sv0 = *(const bf16x8*)(vb_ + koff0); sv1 = *(const bf16x8*)(vb_ + koff1); } while (0)
; #define HLOADK(kt) do { const char* kb_ = (const char*)Kh + (size_t)(kt) * (64 * LDK * 2); sk0 = *(const bf16x8*)(kb_ + koff0); sk1 = *(const bf16x8*)(kb_ + koff1); } while (0)
; #define HWRITEV(b) do { char* d_ = V_lds + (b) * G16_V; *(bf16x8*)(d_ + vst0) = sv0; *(bf16x8*)(d_ + vst1) = sv1; } while (0)
; #define HWRITEK(b) do { char* d_ = K_lds + (b) * GB_K; *(bf16x8*)(d_ + KSWZ(sr, sc * 2)) = sk0; *(bf16x8*)(d_ + KSWZ(32 + sr, sc * 2)) = sk1; } while (0)
; template <int LDQ, int LDK, int LDO>
; __device__ __forceinline__ void attn_gqa16_body(const bf16* __restrict__ Qb, const bf16* __restrict__ Kh, const bf16* __restrict__ Vh, bf16* __restrict__ Ob, int seq, char* lds, float mref) {
;     ...
;   { int l16q = l16, gq = g, widq = wid; asm volatile("" : "+v"(l16q), "+v"(gq), "+v"(widq));
;     const bf16* Qw = Qb + (widq >> 2) * 128 + (long)((widq & 3) * QBLK + l16q) * LDQ + gq * 8;
; #pragma unroll
;     for (int qt = 0; qt < 2; ++qt)
; #pragma unroll
;       for (int ds = 0; ds < 4; ++ds) qr[qt][ds] = *reinterpret_cast<const bf16x8*>(Qw + (long)qt * 16 * LDQ + ds * 32); }
;   const int sr = tid >> 4, sc = (tid & 15) * 8;
;   const int vst0 = (sc >> 4) * VP16 + sr * 32 + ((sc >> 3) & 1) * 16, vst1 = vst0 + 1024;
;   const int vb0 = (int)(uintptr_t)V_lds + (4 * g + (l16 >> 2)) * 32 + (l16 & 3) * 8;
;   const int kb0 = l16 * 272 + g * 16;
;   bf16x8 sv0, sv1, sk0, sk1;
;   const unsigned koff0 = (unsigned)(sr * LDK + sc) * 2u, koff1 = koff0 + 32u * LDK * 2u;
;     ...
;   f32x4a s[4][2]; bf16x8 pb[2][2];
;     ...
;   const int NT = seq / KVBLK;
;   HLOADK(0); HLOADV(0); asm volatile("s_waitcnt vmcnt(0)" ::: "memory"); HWRITEK(0); HWRITEV(0);
;   HLOADK(1); asm volatile("s_waitcnt vmcnt(0)" ::: "memory"); HWRITEK(1); __syncthreads();
;   HLOADK(2); HLOADV(1);
;     ...
;     SBAR(); pv16<4>(o, vb, pb); SBAR();
;     if (more) HEXP();
;   }
;   __builtin_amdgcn_s_setprio(0);
;   ls0 += __shfl_xor(ls0, 16); ls0 += __shfl_xor(ls0, 32); ls1 += __shfl_xor(ls1, 16); ls1 += __shfl_xor(ls1, 32);
;   const float rl[2] = {__builtin_amdgcn_rcpf(ls0), __builtin_amdgcn_rcpf(ls1)};
	ds_read_b64_tr_b16 v[18:19], v184 offset:0x2080
	ds_read_b64_tr_b16 v[20:21], v184 offset:0x2280
	ds_read_b64_tr_b16 v[22:23], v184 offset:0x2480
	ds_read_b64_tr_b16 v[24:25], v184 offset:0x2680
	ds_read_b64_tr_b16 v[70:71], v184 offset:0x28a0
	ds_read_b64_tr_b16 v[72:73], v184 offset:0x2aa0
	ds_read_b64_tr_b16 v[74:75], v184 offset:0x2ca0
	ds_read_b64_tr_b16 v[76:77], v184 offset:0x2ea0
	ds_read_b64_tr_b16 v[106:107], v184 offset:0x30c0
	ds_read_b64_tr_b16 v[108:109], v184 offset:0x32c0
	ds_read_b64_tr_b16 v[110:111], v184 offset:0x34c0
	ds_read_b64_tr_b16 v[112:113], v184 offset:0x36c0
	s_waitcnt lgkmcnt(4)
	s_nop 5
	v_mfma_f32_16x16x32_bf16 v[50:53], v[18:21], v[90:93], v[50:53]
	v_mfma_f32_16x16x32_bf16 v[18:21], v[18:21], v[94:97], v[54:57]
	v_mfma_f32_16x16x32_bf16 v[66:69], v[70:73], v[90:93], v[66:69]
	v_mfma_f32_16x16x32_bf16 v[70:73], v[70:73], v[94:97], v[78:81]
	v_mfma_f32_16x16x32_bf16 v[54:57], v[22:25], v[98:101], v[50:53]
	v_mfma_f32_16x16x32_bf16 v[22:25], v[22:25], v[102:105], v[18:21]
	v_mfma_f32_16x16x32_bf16 v[50:53], v[74:77], v[98:101], v[66:69]
	v_mfma_f32_16x16x32_bf16 v[18:21], v[74:77], v[102:105], v[70:73]
	ds_read_b64_tr_b16 v[66:67], v184 offset:0x38e0
	ds_read_b64_tr_b16 v[68:69], v184 offset:0x3ae0
	ds_read_b64_tr_b16 v[70:71], v184 offset:0x3ce0
	ds_read_b64_tr_b16 v[72:73], v184 offset:0x3ee0
	s_waitcnt lgkmcnt(4)
	v_mfma_f32_16x16x32_bf16 v[26:29], v[106:109], v[90:93], v[26:29]
	s_waitcnt lgkmcnt(0)
	v_mfma_f32_16x16x32_bf16 v[74:77], v[106:109], v[94:97], v[58:61]
	v_mfma_f32_16x16x32_bf16 v[58:61], v[110:113], v[98:101], v[26:29]
	v_mfma_f32_16x16x32_bf16 v[26:29], v[110:113], v[102:105], v[74:77]
	v_mfma_f32_16x16x32_bf16 v[30:33], v[66:69], v[90:93], v[30:33]
	v_mfma_f32_16x16x32_bf16 v[66:69], v[66:69], v[94:97], v[62:65]
	v_mfma_f32_16x16x32_bf16 v[62:65], v[70:73], v[98:101], v[30:33]
	v_mfma_f32_16x16x32_bf16 v[30:33], v[70:73], v[102:105], v[66:69]
	s_nop 5
	v_add_f32_e64 v66, v82, v84
	v_add_f32_e64 v67, v83, v85
	v_pk_add_f32 v[68:69], v[114:115], v[114:115] op_sel:[0,1] op_sel_hi:[1,0]
	v_pk_add_f32 v[66:67], v[66:67], v[66:67] op_sel:[0,1] op_sel_hi:[1,0]
	v_add_f32_e32 v86, v88, v116
	v_add_f32_e32 v88, v117, v118
	v_mov_b32_e32 v69, v119
	v_mov_b32_e32 v67, v120
	v_pk_add_f32 v[66:67], v[68:69], v[66:67]
	v_pk_add_f32 v[68:69], v[86:87], v[88:89]
	s_nop 0
	v_pk_add_f32 v[66:67], v[66:67], v[68:69]
	s_nop 0
	v_add_f32_e32 v66, v66, v67
	s_setprio 0
	ds_bpermute_b32 v67, v177, v66
	ds_bpermute_b32 v68, v177, v121
	v_mov_b32_e32 v70, v185
	s_mov_b64 s[14:15], 0
	s_waitcnt lgkmcnt(1)
	v_add_f32_e32 v66, v66, v67
	s_waitcnt lgkmcnt(0)
	v_add_f32_e32 v67, v121, v68
	ds_bpermute_b32 v68, v188, v66
	ds_bpermute_b32 v69, v188, v67
	s_waitcnt lgkmcnt(1)
	v_add_f32_e32 v66, v66, v68
	s_waitcnt lgkmcnt(0)
	v_add_f32_e32 v67, v67, v69
	v_rcp_f32_e32 v68, v66
	v_rcp_f32_e32 v66, v67
	v_mov_b32_e32 v67, v176
	v_mov_b32_e32 v69, v180
.LBB0_646:
	s_and_b64 vcc, exec, s[14:15]
	s_cbranch_vccz .LBB0_641
	s_lshl_b32 s8, s45, 7
	s_and_b32 s8, s8, 0x3f80
	s_ashr_i32 s14, s45, 8
	s_mul_i32 s12, s8, 0x2400
	s_add_u32 s15, s33, s12
	s_addc_u32 s17, s35, 0
	s_lshl_b32 s13, s45, 1
	s_lshl_b32 s12, s14, 9
	s_and_b32 s13, s13, 0x100
	s_or_b32 s12, s12, s13
	s_ashr_i32 s13, s12, 31
	v_mov_b32_e32 v4, v180
	v_mov_b32_e32 v2, v185
	v_mov_b32_e32 v5, v176
	s_lshl_b64 s[12:13], s[12:13], 1
	s_add_u32 s16, s15, s12
	v_lshlrev_b32_e32 v6, 5, v2
	v_and_b32_e32 v2, 0xffffff80, v6
	s_addc_u32 s17, s17, s13
	v_ashrrev_i32_e32 v3, 31, v2
	v_and_b32_e32 v6, 0x60, v6
	s_lshl_b32 s14, s14, 7
	v_lshl_add_u64 v[2:3], v[2:3], 1, s[16:17]
	v_add_u32_e32 v4, v6, v4
	s_ashr_i32 s15, s14, 31
	v_mad_i64_i32 v[2:3], s[16:17], v4, s26, v[2:3]
	v_lshlrev_b32_e32 v4, 3, v5
	s_lshl_b64 s[46:47], s[14:15], 1
	v_ashrrev_i32_e32 v5, 31, v4
	s_add_u32 s48, s21, s46
	v_lshl_add_u64 v[6:7], v[4:5], 1, v[2:3]
	s_addc_u32 s49, s22, s47
	global_load_dwordx4 v[30:33], v[6:7], off
	global_load_dwordx4 v[18:21], v[6:7], off offset:64
	global_load_dwordx4 v[10:13], v[6:7], off offset:128
	global_load_dwordx4 v[2:5], v[6:7], off offset:192
	v_add_co_u32_e32 v6, vcc, s27, v6
	s_add_u32 s46, s23, s46
	s_nop 0
	v_addc_co_u32_e32 v7, vcc, 0, v7, vcc
	v_lshl_add_u64 v[102:103], s[48:49], 0, v[178:179]
	s_addc_u32 s47, s24, s47
	s_add_u32 s74, s46, 0x90000
	s_addc_u32 s75, s47, 0
	s_add_u32 s76, s74, 0x48000
	s_addc_u32 s77, s75, 0
	v_add_co_u32_e32 v34, vcc, s28, v102
	v_lshl_add_u64 v[104:105], s[46:47], 0, v[178:179]
	s_nop 0
	v_addc_co_u32_e32 v35, vcc, 0, v103, vcc
	v_add_co_u32_e32 v46, vcc, s28, v104
	global_load_dwordx4 v[38:41], v[6:7], off
	global_load_dwordx4 v[22:25], v[6:7], off offset:64
	global_load_dwordx4 v[14:17], v[6:7], off offset:128
	s_nop 0
	global_load_dwordx4 v[6:9], v[6:7], off offset:192
	v_addc_co_u32_e32 v47, vcc, 0, v105, vcc
	v_add_co_u32_e32 v50, vcc, s29, v102
	global_load_dwordx4 v[26:29], v[102:103], off
	s_nop 0
	global_load_dwordx4 v[34:37], v[34:35], off
	v_addc_co_u32_e32 v51, vcc, 0, v103, vcc
	v_add_co_u32_e32 v54, vcc, s30, v102
	global_load_dwordx4 v[42:45], v[104:105], off
	s_nop 0
	global_load_dwordx4 v[46:49], v[46:47], off
	s_waitcnt vmcnt(0)
	v_addc_co_u32_e32 v55, vcc, 0, v103, vcc
	global_load_dwordx4 v[50:53], v[50:51], off
	s_nop 0
	global_load_dwordx4 v[54:57], v[54:55], off
	s_waitcnt vmcnt(5)
	ds_write_b128 v194, v[26:29] offset:33280
	s_waitcnt vmcnt(4)
	ds_write_b128 v194, v[34:37] offset:41984
	s_waitcnt vmcnt(3)
	ds_write_b128 v181, v[42:45]
	s_waitcnt vmcnt(2)
	ds_write_b128 v181, v[46:49] offset:1024
	s_waitcnt vmcnt(0)
	s_waitcnt vmcnt(1)
	ds_write_b128 v194, v[50:53] offset:50688
	s_waitcnt vmcnt(0)
	ds_write_b128 v194, v[54:57] offset:59392
	s_waitcnt lgkmcnt(0)
	s_barrier
; #define HLOADV(kt) do { const char* vb_ = (const char*)Vh + (size_t)(kt) * (64 * LDK * 2); sv0 = *(const bf16x8*)(vb_ + koff0); sv1 = *(const bf16x8*)(vb_ + koff1); } while (0)
; #define HLOADK(kt) do { const char* kb_ = (const char*)Kh + (size_t)(kt) * (64 * LDK * 2); sk0 = *(const bf16x8*)(kb_ + koff0); sk1 = *(const bf16x8*)(kb_ + koff1); } while (0)
; #define HWRITEV(b) do { char* d_ = V_lds + (b) * G16_V; *(bf16x8*)(d_ + vst0) = sv0; *(bf16x8*)(d_ + vst1) = sv1; } while (0)
; #define HWRITEK(b) do { char* d_ = K_lds + (b) * GB_K; *(bf16x8*)(d_ + KSWZ(sr, sc * 2)) = sk0; *(bf16x8*)(d_ + KSWZ(32 + sr, sc * 2)) = sk1; } while (0)
; #define HEXP() do { _Pragma("unroll") for (int kt = 0; kt < 4; ++kt) { _Pragma("unroll") for (int qt = 0; qt < 2; ++qt) { _Pragma("unroll") for (int i = 0; i < 4; ++i) s[kt][qt][i] = __builtin_amdgcn_exp2f(fmaf(s[kt][qt][i], C, mnC)); } } } while (0)
; template <int LDQ, int LDK, int LDO>
; __device__ __forceinline__ void attn_gqa16_body(const bf16* __restrict__ Qb, const bf16* __restrict__ Kh, const bf16* __restrict__ Vh, bf16* __restrict__ Ob, int seq, char* lds, float mref) {
;     ...
;   float ls0 = 0.f, ls1 = 0.f; f32x4a o[8][2] = {}; bf16x8 qr[2][4];
;   { int l16q = l16, gq = g, widq = wid; asm volatile("" : "+v"(l16q), "+v"(gq), "+v"(widq));
;     const bf16* Qw = Qb + (widq >> 2) * 128 + (long)((widq & 3) * QBLK + l16q) * LDQ + gq * 8;
; #pragma unroll
;     for (int qt = 0; qt < 2; ++qt)
; #pragma unroll
;       for (int ds = 0; ds < 4; ++ds) qr[qt][ds] = *reinterpret_cast<const bf16x8*>(Qw + (long)qt * 16 * LDQ + ds * 32); }
;   const int sr = tid >> 4, sc = (tid & 15) * 8;
;   const int vst0 = (sc >> 4) * VP16 + sr * 32 + ((sc >> 3) & 1) * 16, vst1 = vst0 + 1024;
;   const int vb0 = (int)(uintptr_t)V_lds + (4 * g + (l16 >> 2)) * 32 + (l16 & 3) * 8;
;   const int kb0 = l16 * 272 + g * 16;
;   bf16x8 sv0, sv1, sk0, sk1;
;   const unsigned koff0 = (unsigned)(sr * LDK + sc) * 2u, koff1 = koff0 + 32u * LDK * 2u;
;     ...
;   f32x4a s[4][2]; bf16x8 pb[2][2];
;     ...
;   const int NT = seq / KVBLK;
;   HLOADK(0); HLOADV(0); asm volatile("s_waitcnt vmcnt(0)" ::: "memory"); HWRITEK(0); HWRITEV(0);
;   HLOADK(1); asm volatile("s_waitcnt vmcnt(0)" ::: "memory"); HWRITEK(1); __syncthreads();
;   HLOADK(2); HLOADV(1);
;   HQK(0); HEXP();
;   if (wid >= 4) __builtin_amdgcn_s_setprio(1);
;   for (int t = 0; t < NT; ++t) {
	ds_read_b128 v[26:29], v182 offset:33280
	ds_read_b128 v[34:37], v182 offset:33344
	ds_read_b128 v[46:49], v182 offset:37632
	ds_read_b128 v[50:53], v182 offset:37696
	ds_read_b128 v[58:61], v182 offset:41984
	ds_read_b128 v[62:65], v182 offset:42048
	ds_read_b128 v[70:73], v182 offset:46336
	ds_read_b128 v[74:77], v182 offset:46400
	s_waitcnt lgkmcnt(7)
	v_mfma_f32_16x16x32_bf16 v[42:45], v[26:29], v[30:33], 0
	v_mfma_f32_16x16x32_bf16 v[26:29], v[26:29], v[38:41], 0
	s_waitcnt lgkmcnt(5)
	v_mfma_f32_16x16x32_bf16 v[54:57], v[46:49], v[30:33], 0
	v_mfma_f32_16x16x32_bf16 v[46:49], v[46:49], v[38:41], 0
	s_waitcnt lgkmcnt(3)
	v_mfma_f32_16x16x32_bf16 v[66:69], v[58:61], v[30:33], 0
	v_mfma_f32_16x16x32_bf16 v[58:61], v[58:61], v[38:41], 0
	s_waitcnt lgkmcnt(1)
	v_mfma_f32_16x16x32_bf16 v[78:81], v[70:73], v[30:33], 0
	v_mfma_f32_16x16x32_bf16 v[70:73], v[70:73], v[38:41], 0
	v_mfma_f32_16x16x32_bf16 v[42:45], v[34:37], v[18:21], v[42:45]
	v_mfma_f32_16x16x32_bf16 v[26:29], v[34:37], v[22:25], v[26:29]
	v_mfma_f32_16x16x32_bf16 v[34:37], v[50:53], v[18:21], v[54:57]
	v_mfma_f32_16x16x32_bf16 v[46:49], v[50:53], v[22:25], v[46:49]
	v_mfma_f32_16x16x32_bf16 v[50:53], v[62:65], v[18:21], v[66:69]
	v_mfma_f32_16x16x32_bf16 v[54:57], v[62:65], v[22:25], v[58:61]
	s_waitcnt lgkmcnt(0)
	v_mfma_f32_16x16x32_bf16 v[58:61], v[74:77], v[18:21], v[78:81]
	v_mfma_f32_16x16x32_bf16 v[62:65], v[74:77], v[22:25], v[70:73]
	ds_read_b128 v[66:69], v182 offset:33408
	ds_read_b128 v[74:77], v182 offset:33472
	s_waitcnt lgkmcnt(1)
	v_mfma_f32_16x16x32_bf16 v[42:45], v[66:69], v[10:13], v[42:45]
	v_mfma_f32_16x16x32_bf16 v[26:29], v[66:69], v[14:17], v[26:29]
	ds_read_b128 v[66:69], v182 offset:37760
	ds_read_b128 v[78:81], v182 offset:37824
	s_waitcnt lgkmcnt(1)
	v_mfma_f32_16x16x32_bf16 v[34:37], v[66:69], v[10:13], v[34:37]
	v_mfma_f32_16x16x32_bf16 v[46:49], v[66:69], v[14:17], v[46:49]
	ds_read_b128 v[66:69], v182 offset:42112
	ds_read_b128 v[82:85], v182 offset:42176
	s_waitcnt lgkmcnt(1)
	v_mfma_f32_16x16x32_bf16 v[50:53], v[66:69], v[10:13], v[50:53]
	v_mfma_f32_16x16x32_bf16 v[86:89], v[66:69], v[14:17], v[54:57]
	s_nop 2
	ds_read_b128 v[54:57], v182 offset:46464
	ds_read_b128 v[90:93], v182 offset:46528
	v_mfma_f32_16x16x32_bf16 v[66:69], v[74:77], v[6:9], v[26:29]
	s_nop 2
	v_add_co_u32_e32 v26, vcc, s25, v102
	s_waitcnt lgkmcnt(1)
	v_mfma_f32_16x16x32_bf16 v[98:101], v[54:57], v[14:17], v[62:65]
	v_addc_co_u32_e32 v27, vcc, 0, v103, vcc
	v_add_co_u32_e32 v28, vcc, s31, v102
	v_mfma_f32_16x16x32_bf16 v[62:65], v[78:81], v[2:5], v[34:37]
	s_nop 0
	v_addc_co_u32_e32 v29, vcc, 0, v103, vcc
	global_load_dwordx4 v[106:109], v[26:27], off
	global_load_dwordx4 v[110:113], v[28:29], off
	v_add_co_u32_e32 v26, vcc, s29, v104
	v_mfma_f32_16x16x32_bf16 v[94:97], v[54:57], v[10:13], v[58:61]
	s_nop 0
	v_addc_co_u32_e32 v27, vcc, 0, v105, vcc
	v_add_co_u32_e32 v34, vcc, s30, v104
	v_mfma_f32_16x16x32_bf16 v[70:73], v[74:77], v[2:5], v[42:45]
	s_nop 0
	v_addc_co_u32_e32 v35, vcc, 0, v105, vcc
	s_nop 0
	v_mfma_f32_16x16x32_bf16 v[58:61], v[78:81], v[6:9], v[46:49]
	v_mfma_f32_16x16x32_bf16 v[54:57], v[82:85], v[2:5], v[50:53]
	v_mfma_f32_16x16x32_bf16 v[50:53], v[82:85], v[6:9], v[86:89]
	s_waitcnt lgkmcnt(0)
	v_mfma_f32_16x16x32_bf16 v[46:49], v[90:93], v[2:5], v[94:97]
	v_mfma_f32_16x16x32_bf16 v[42:45], v[90:93], v[6:9], v[98:101]
	s_and_saveexec_b64 s[16:17], s[4:5]
	s_setprio 1
	s_or_b64 exec, exec, s[16:17]
	v_add_f32_e32 v70, v186, v70
	v_add_f32_e32 v66, v186, v66
	v_add_f32_e32 v62, v186, v62
	v_add_f32_e32 v58, v186, v58
	v_add_f32_e32 v54, v186, v54
	v_add_f32_e32 v50, v186, v50
	v_add_f32_e32 v46, v186, v46
	v_add_f32_e32 v42, v186, v42
	v_exp_f32_e32 v158, v70
	v_add_f32_e32 v70, v186, v71
	v_exp_f32_e32 v159, v66
	v_add_f32_e32 v66, v186, v67
	v_exp_f32_e32 v168, v62
	v_add_f32_e32 v62, v186, v63
	v_exp_f32_e32 v169, v58
	v_add_f32_e32 v58, v186, v59
	v_exp_f32_e32 v142, v54
	v_add_f32_e32 v54, v186, v55
	v_exp_f32_e32 v143, v50
	v_add_f32_e32 v50, v186, v51
	v_exp_f32_e32 v134, v46
	v_add_f32_e32 v46, v186, v47
	v_exp_f32_e32 v135, v42
	v_add_f32_e32 v42, v186, v43
	v_exp_f32_e32 v152, v70
	v_add_f32_e32 v70, v186, v72
	v_exp_f32_e32 v153, v66
	v_add_f32_e32 v66, v186, v68
	v_exp_f32_e32 v170, v62
	v_add_f32_e32 v62, v186, v64
	v_exp_f32_e32 v171, v58
	v_add_f32_e32 v58, v186, v60
	v_exp_f32_e32 v172, v54
	v_add_f32_e32 v54, v186, v56
	v_exp_f32_e32 v173, v50
	v_add_f32_e32 v50, v186, v52
	v_exp_f32_e32 v138, v46
	v_add_f32_e32 v46, v186, v48
	v_exp_f32_e32 v139, v42
	v_add_f32_e32 v42, v186, v44
	v_exp_f32_e32 v156, v70
	v_add_f32_e32 v70, v186, v73
	v_exp_f32_e32 v157, v66
	v_add_f32_e32 v66, v186, v69
	v_exp_f32_e32 v164, v62
	v_add_f32_e32 v62, v186, v65
	v_exp_f32_e32 v165, v58
	v_add_f32_e32 v58, v186, v61
	v_exp_f32_e32 v144, v54
	v_add_f32_e32 v54, v186, v57
	v_exp_f32_e32 v145, v50
	v_add_f32_e32 v50, v186, v53
	v_exp_f32_e32 v136, v46
	v_add_f32_e32 v46, v186, v49
	v_exp_f32_e32 v137, v42
	v_add_f32_e32 v42, v186, v45
	v_exp_f32_e32 v160, v70
	v_exp_f32_e32 v161, v66
	v_exp_f32_e32 v166, v62
	v_exp_f32_e32 v167, v58
	v_exp_f32_e32 v174, v54
	v_exp_f32_e32 v175, v50
	v_exp_f32_e32 v140, v46
	v_exp_f32_e32 v141, v42
	v_mov_b32_e32 v50, 0
	v_lshl_add_u64 v[162:163], s[14:15], 1, v[154:155]
	s_mov_b32 s16, 0
	s_mov_b64 s[14:15], 0
	v_mov_b32_e32 v51, v50
	v_mov_b32_e32 v52, v50
	v_mov_b32_e32 v53, v50
	v_mov_b32_e32 v78, v50
	v_mov_b32_e32 v79, v50
	v_mov_b32_e32 v80, v50
	v_mov_b32_e32 v81, v50
	v_mov_b32_e32 v90, v50
	v_mov_b32_e32 v91, v50
	v_mov_b32_e32 v92, v50
	v_mov_b32_e32 v93, v50
	v_mov_b32_e32 v94, v50
	v_mov_b32_e32 v95, v50
	v_mov_b32_e32 v96, v50
	v_mov_b32_e32 v97, v50
	v_mov_b32_e32 v98, v50
	v_mov_b32_e32 v99, v50
	v_mov_b32_e32 v100, v50
	v_mov_b32_e32 v101, v50
	v_mov_b32_e32 v102, v50
	v_mov_b32_e32 v103, v50
	v_mov_b32_e32 v104, v50
	v_mov_b32_e32 v105, v50
	v_mov_b32_e32 v82, v50
	v_mov_b32_e32 v83, v50
	v_mov_b32_e32 v84, v50
	v_mov_b32_e32 v85, v50
	v_mov_b32_e32 v86, v50
	v_mov_b32_e32 v87, v50
	v_mov_b32_e32 v88, v50
	v_mov_b32_e32 v89, v50
	v_mov_b32_e32 v54, v50
	v_mov_b32_e32 v55, v50
	v_mov_b32_e32 v56, v50
	v_mov_b32_e32 v57, v50
	v_mov_b32_e32 v62, v50
	v_mov_b32_e32 v63, v50
	v_mov_b32_e32 v64, v50
	v_mov_b32_e32 v65, v50
	v_mov_b32_e32 v58, v50
	v_mov_b32_e32 v59, v50
	v_mov_b32_e32 v60, v50
	v_mov_b32_e32 v61, v50
	v_mov_b32_e32 v70, v50
	v_mov_b32_e32 v71, v50
	v_mov_b32_e32 v72, v50
	v_mov_b32_e32 v73, v50
	v_mov_b32_e32 v42, v50
	v_mov_b32_e32 v43, v50
	v_mov_b32_e32 v44, v50
	v_mov_b32_e32 v45, v50
	v_mov_b32_e32 v46, v50
	v_mov_b32_e32 v47, v50
	v_mov_b32_e32 v48, v50
	v_mov_b32_e32 v49, v50
	v_mov_b32_e32 v66, v50
	v_mov_b32_e32 v67, v50
	v_mov_b32_e32 v68, v50
	v_mov_b32_e32 v69, v50
	v_mov_b32_e32 v74, v50
	v_mov_b32_e32 v75, v50
	v_mov_b32_e32 v76, v50
	v_mov_b32_e32 v77, v50
	v_mov_b32_e32 v150, v50
	v_mov_b32_e32 v151, v50
	s_nop 0
	s_nop 0
	s_nop 0
	s_nop 0
	s_nop 0
	s_nop 0
	s_nop 0
	s_nop 0
	s_nop 0
	s_nop 0
	s_nop 0
	s_nop 0
	s_nop 0
	s_nop 0
	s_nop 0
; #define SBAR() __builtin_amdgcn_sched_barrier(0)
; template <int LDQ, int LDK, int LDO>
; __device__ __forceinline__ void attn_gqa16_body(const bf16* __restrict__ Qb, const bf16* __restrict__ Kh, const bf16* __restrict__ Vh, bf16* __restrict__ Ob, int seq, char* lds, float mref) {
;     ...
;   for (int t = 0; t < NT; ++t) {
;     HPACK();
;     __syncthreads();
;     const bool more = t + 1 < NT;
;     if (more) HQK((t + 1) & 1);
;     const int vb = vb0 + (t & 1) * (int)G16_V;
;     SBAR(); pv16<0>(o, vb, pb); SBAR();
.LBB0_650:
	s_add_i32 s17, s16, 1
	s_and_b32 s16, s16, 1
	s_and_b32 s46, 1, s17
	s_cmp_eq_u32 s46, 1
	s_cselect_b32 s85, s86, s84
	s_cselect_b32 s46, 0x4400, 0
	v_add_u32_e32 v189, s46, v182
	v_cvt_pk_bf16_f32 v114, v158, v152
	v_cvt_pk_bf16_f32 v115, v156, v160
	v_cvt_pk_bf16_f32 v116, v168, v170
	v_cvt_pk_bf16_f32 v117, v164, v166
	v_cvt_pk_bf16_f32 v118, v159, v153
	v_cvt_pk_bf16_f32 v119, v157, v161
	v_cvt_pk_bf16_f32 v120, v169, v171
	v_cvt_pk_bf16_f32 v121, v165, v167
	v_cvt_pk_bf16_f32 v122, v142, v172
	v_cvt_pk_bf16_f32 v123, v144, v174
	v_cvt_pk_bf16_f32 v124, v134, v138
	v_cvt_pk_bf16_f32 v125, v136, v140
	v_cvt_pk_bf16_f32 v126, v143, v173
	v_cvt_pk_bf16_f32 v127, v145, v175
	v_cvt_pk_bf16_f32 v128, v135, v139
	v_cvt_pk_bf16_f32 v129, v137, v141
	s_waitcnt vmcnt(2)
	s_barrier
	ds_read_b128 v[130:133], v189 offset:33280
	ds_read_b128 v[146:149], v189 offset:33344
	ds_read_b128 v[200:203], v189 offset:37632
	ds_read_b128 v[204:207], v189 offset:37696
	ds_read_b128 v[212:215], v189 offset:41984
	ds_read_b128 v[216:219], v189 offset:42048
	ds_read_b128 v[224:227], v189 offset:46336
	ds_read_b128 v[228:231], v189 offset:46400
	s_mov_b32 m0, s85
	s_nop 0
	global_load_lds_dwordx4 v253, s[74:75]
	s_add_i32 m0, s85, 0x400
	s_nop 0
	global_load_lds_dwordx4 v253, s[76:77]
	s_add_u32 s74, s74, 0x90000
	s_addc_u32 s75, s75, 0
	s_add_u32 s76, s76, 0x90000
	s_addc_u32 s77, s77, 0
	s_waitcnt lgkmcnt(7)
	v_mfma_f32_16x16x32_bf16 v[196:199], v[130:133], v[30:33], v[248:251]
	v_add_f32_e64 v134, v134, v138
	v_add_f32_e64 v135, v135, v139
	v_pk_add_f32 v[136:137], v[136:137], v[140:141]
	s_mul_i32 s46, s16, 0x4100
	v_mfma_f32_16x16x32_bf16 v[130:133], v[130:133], v[38:41], v[248:251]
	s_waitcnt lgkmcnt(5)
	v_mfma_f32_16x16x32_bf16 v[208:211], v[200:203], v[30:33], v[248:251]
	v_mfma_f32_16x16x32_bf16 v[200:203], v[200:203], v[38:41], v[248:251]
	s_waitcnt lgkmcnt(3)
	v_mfma_f32_16x16x32_bf16 v[220:223], v[212:215], v[30:33], v[248:251]
	v_mfma_f32_16x16x32_bf16 v[212:215], v[212:215], v[38:41], v[248:251]
	s_waitcnt lgkmcnt(1)
	v_mfma_f32_16x16x32_bf16 v[232:235], v[224:227], v[30:33], v[248:251]
	v_mfma_f32_16x16x32_bf16 v[224:227], v[224:227], v[38:41], v[248:251]
	v_mfma_f32_16x16x32_bf16 v[196:199], v[146:149], v[18:21], v[196:199]
	v_mfma_f32_16x16x32_bf16 v[130:133], v[146:149], v[22:25], v[130:133]
	v_mfma_f32_16x16x32_bf16 v[146:149], v[204:207], v[18:21], v[208:211]
	v_mfma_f32_16x16x32_bf16 v[200:203], v[204:207], v[22:25], v[200:203]
	v_mfma_f32_16x16x32_bf16 v[204:207], v[216:219], v[18:21], v[220:223]
	v_mfma_f32_16x16x32_bf16 v[208:211], v[216:219], v[22:25], v[212:215]
	s_waitcnt lgkmcnt(0)
	v_mfma_f32_16x16x32_bf16 v[216:219], v[228:231], v[22:25], v[224:227]
	ds_read_b128 v[220:223], v189 offset:33408
	s_nop 1
	ds_read_b128 v[224:227], v189 offset:33472
	v_mfma_f32_16x16x32_bf16 v[212:215], v[228:231], v[18:21], v[232:235]
	s_waitcnt lgkmcnt(1)
	v_mfma_f32_16x16x32_bf16 v[196:199], v[220:223], v[10:13], v[196:199]
	v_mfma_f32_16x16x32_bf16 v[130:133], v[220:223], v[14:17], v[130:133]
	ds_read_b128 v[220:223], v189 offset:37760
	ds_read_b128 v[228:231], v189 offset:37824
	s_waitcnt lgkmcnt(1)
	v_mfma_f32_16x16x32_bf16 v[146:149], v[220:223], v[10:13], v[146:149]
	v_mfma_f32_16x16x32_bf16 v[200:203], v[220:223], v[14:17], v[200:203]
	ds_read_b128 v[220:223], v189 offset:42112
	ds_read_b128 v[232:235], v189 offset:42176
	s_waitcnt lgkmcnt(1)
	v_mfma_f32_16x16x32_bf16 v[204:207], v[220:223], v[10:13], v[204:207]
	v_mfma_f32_16x16x32_bf16 v[208:211], v[220:223], v[14:17], v[208:211]
	ds_read_b128 v[220:223], v189 offset:46464
	ds_read_b128 v[236:239], v189 offset:46528
	v_add_u32_e32 v189, s46, v183
	s_waitcnt lgkmcnt(1)
	v_mfma_f32_16x16x32_bf16 v[212:215], v[220:223], v[10:13], v[212:215]
	v_mfma_f32_16x16x32_bf16 v[216:219], v[220:223], v[14:17], v[216:219]
	v_mfma_f32_16x16x32_bf16 v[220:223], v[224:227], v[6:9], v[130:133]
	s_nop 2
	v_add_f32_e64 v130, v158, v152
	v_add_f32_e64 v131, v159, v153
	v_pk_add_f32 v[132:133], v[156:157], v[160:161]
	v_pk_add_f32 v[152:153], v[168:169], v[170:171]
	v_pk_add_f32 v[156:157], v[164:165], v[166:167]
	v_pk_add_f32 v[158:159], v[142:143], v[172:173]
	v_pk_add_f32 v[160:161], v[144:145], v[174:175]
	v_pk_add_f32 v[130:131], v[130:131], v[132:133]
	v_mfma_f32_16x16x32_bf16 v[142:145], v[232:235], v[2:5], v[204:207]
	v_add_f32_e64 v152, v152, v156
	v_add_f32_e64 v153, v153, v157
	v_pk_add_f32 v[156:157], v[158:159], v[160:161]
	v_pk_add_f32 v[158:159], v[134:135], v[136:137]
	v_mfma_f32_16x16x32_bf16 v[138:141], v[232:235], v[6:9], v[208:211]
	v_add_f32_e64 v150, v150, v130
	v_add_f32_e64 v151, v151, v131
	v_pk_add_f32 v[150:151], v[152:153], v[150:151]
	s_waitcnt lgkmcnt(0)
	v_mfma_f32_16x16x32_bf16 v[134:137], v[236:239], v[2:5], v[212:215]
	v_add_f32_e64 v150, v156, v150
	v_add_f32_e64 v151, v157, v151
	v_pk_add_f32 v[150:151], v[158:159], v[150:151]
	v_mfma_f32_16x16x32_bf16 v[196:199], v[224:227], v[2:5], v[196:199]
	v_mfma_f32_16x16x32_bf16 v[224:227], v[228:231], v[2:5], v[146:149]
	v_mfma_f32_16x16x32_bf16 v[146:149], v[228:231], v[6:9], v[200:203]
	v_mfma_f32_16x16x32_bf16 v[130:133], v[236:239], v[6:9], v[216:219]
	ds_read_b64_tr_b16 v[156:157], v189 offset:0
	ds_read_b64_tr_b16 v[158:159], v189 offset:0x200
	ds_read_b64_tr_b16 v[164:165], v189 offset:0x400
	ds_read_b64_tr_b16 v[166:167], v189 offset:0x600
	ds_read_b64_tr_b16 v[168:169], v189 offset:0x820
	ds_read_b64_tr_b16 v[170:171], v189 offset:0xa20
	ds_read_b64_tr_b16 v[172:173], v189 offset:0xc20
	ds_read_b64_tr_b16 v[174:175], v189 offset:0xe20
	ds_read_b64_tr_b16 v[200:201], v189 offset:0x1040
	ds_read_b64_tr_b16 v[202:203], v189 offset:0x1240
	ds_read_b64_tr_b16 v[204:205], v189 offset:0x1440
	ds_read_b64_tr_b16 v[206:207], v189 offset:0x1640
	s_waitcnt lgkmcnt(4)
; #define SBAR() __builtin_amdgcn_sched_barrier(0)
; #define MFMA16(a, b, c) __builtin_amdgcn_mfma_f32_16x16x32_bf16(a, b, c, 0, 0, 0)
; template <int D0> __device__ __forceinline__ void pv16(f32x4a (&o)[8][2], int vb, const bf16x8 (&pb)[2][2]) {
;     ...
;   const s16x4 a0 = TR(D0, 0, 0), a1 = TR(D0, 0, 1), a2 = TR(D0, 1, 0), a3 = TR(D0, 1, 1), b0 = TR(D0 + 1, 0, 0), b1 = TR(D0 + 1, 0, 1), b2 = TR(D0 + 1, 1, 0), b3 = TR(D0 + 1, 1, 1);
;   const s16x4 c0 = TR(D0 + 2, 0, 0), c1 = TR(D0 + 2, 0, 1), c2 = TR(D0 + 2, 1, 0), c3 = TR(D0 + 2, 1, 1);
;   asm volatile("s_waitcnt lgkmcnt(4)" ::: "memory"); SBAR();
;   o[D0][0] = MFMA16(PK16(a0, a1), pb[0][0], o[D0][0]); o[D0][1] = MFMA16(PK16(a0, a1), pb[0][1], o[D0][1]);
;   o[D0 + 1][0] = MFMA16(PK16(b0, b1), pb[0][0], o[D0 + 1][0]); o[D0 + 1][1] = MFMA16(PK16(b0, b1), pb[0][1], o[D0 + 1][1]);
;   o[D0][0] = MFMA16(PK16(a2, a3), pb[1][0], o[D0][0]); o[D0][1] = MFMA16(PK16(a2, a3), pb[1][1], o[D0][1]);
;   o[D0 + 1][0] = MFMA16(PK16(b2, b3), pb[1][0], o[D0 + 1][0]); o[D0 + 1][1] = MFMA16(PK16(b2, b3), pb[1][1], o[D0 + 1][1]);
;   SBAR();
;   const s16x4 d0 = TR(D0 + 3, 0, 0), d1 = TR(D0 + 3, 0, 1), d2 = TR(D0 + 3, 1, 0), d3 = TR(D0 + 3, 1, 1);
;   asm volatile("s_waitcnt lgkmcnt(4)" ::: "memory"); SBAR();
;   o[D0 + 2][0] = MFMA16(PK16(c0, c1), pb[0][0], o[D0 + 2][0]); o[D0 + 2][1] = MFMA16(PK16(c0, c1), pb[0][1], o[D0 + 2][1]);
;   o[D0 + 2][0] = MFMA16(PK16(c2, c3), pb[1][0], o[D0 + 2][0]); o[D0 + 2][1] = MFMA16(PK16(c2, c3), pb[1][1], o[D0 + 2][1]);
;   asm volatile("s_waitcnt lgkmcnt(0)" ::: "memory"); SBAR();
;   o[D0 + 3][0] = MFMA16(PK16(d0, d1), pb[0][0], o[D0 + 3][0]); o[D0 + 3][1] = MFMA16(PK16(d0, d1), pb[0][1], o[D0 + 3][1]);
;   o[D0 + 3][0] = MFMA16(PK16(d2, d3), pb[1][0], o[D0 + 3][0]); o[D0 + 3][1] = MFMA16(PK16(d2, d3), pb[1][1], o[D0 + 3][1]);
; template <int LDQ, int LDK, int LDO>
; __device__ __forceinline__ void attn_gqa16_body(const bf16* __restrict__ Qb, const bf16* __restrict__ Kh, const bf16* __restrict__ Vh, bf16* __restrict__ Ob, int seq, char* lds, float mref) {
;     ...
;     asm volatile("s_waitcnt vmcnt(0)" ::: "memory");
;     if (t + 2 < NT) HWRITEK(t & 1);
;     if (t + 1 < NT) HWRITEV((t + 1) & 1);
;     HLOADK(t + 3); HLOADV(t + 2);
;     SBAR(); pv16<4>(o, vb, pb); SBAR();
;     if (more) HEXP();
;   }
	s_nop 0
	v_mfma_f32_16x16x32_bf16 v[102:105], v[156:159], v[114:117], v[102:105]
	v_mfma_f32_16x16x32_bf16 v[98:101], v[156:159], v[118:121], v[98:101]
	v_mfma_f32_16x16x32_bf16 v[94:97], v[168:171], v[114:117], v[94:97]
	v_mfma_f32_16x16x32_bf16 v[90:93], v[168:171], v[118:121], v[90:93]
	v_mfma_f32_16x16x32_bf16 v[102:105], v[164:167], v[122:125], v[102:105]
	v_mfma_f32_16x16x32_bf16 v[98:101], v[164:167], v[126:129], v[98:101]
	v_mfma_f32_16x16x32_bf16 v[94:97], v[172:175], v[122:125], v[94:97]
	v_mfma_f32_16x16x32_bf16 v[90:93], v[172:175], v[126:129], v[90:93]
	ds_read_b64_tr_b16 v[156:157], v189 offset:0x1860
	ds_read_b64_tr_b16 v[158:159], v189 offset:0x1a60
	ds_read_b64_tr_b16 v[164:165], v189 offset:0x1c60
	ds_read_b64_tr_b16 v[166:167], v189 offset:0x1e60
	s_waitcnt lgkmcnt(4)
	v_mfma_f32_16x16x32_bf16 v[78:81], v[200:203], v[114:117], v[78:81]
	s_waitcnt lgkmcnt(0)
	v_mfma_f32_16x16x32_bf16 v[50:53], v[200:203], v[118:121], v[50:53]
	v_mfma_f32_16x16x32_bf16 v[78:81], v[204:207], v[122:125], v[78:81]
	v_mfma_f32_16x16x32_bf16 v[50:53], v[204:207], v[126:129], v[50:53]
	v_mfma_f32_16x16x32_bf16 v[82:85], v[156:159], v[114:117], v[82:85]
	v_mfma_f32_16x16x32_bf16 v[86:89], v[156:159], v[118:121], v[86:89]
	v_mfma_f32_16x16x32_bf16 v[82:85], v[164:167], v[122:125], v[82:85]
	v_mfma_f32_16x16x32_bf16 v[86:89], v[164:167], v[126:129], v[86:89]
	v_lshl_add_u64 v[152:153], v[162:163], 0, s[14:15]
	v_add_co_u32_e32 v156, vcc, s37, v152
	s_mulk_i32 s16, 0x4400
	s_nop 0
	v_addc_co_u32_e32 v157, vcc, 0, v153, vcc
	v_add_co_u32_e32 v158, vcc, s38, v152
	v_add_u32_e32 v164, s16, v194
	s_nop 0
	v_addc_co_u32_e32 v159, vcc, 0, v153, vcc
	s_waitcnt vmcnt(2)
	ds_write_b128 v164, v[106:109] offset:33280
	ds_write_b128 v164, v[110:113] offset:41984
	global_load_dwordx4 v[106:109], v[156:157], off offset:3072
	global_load_dwordx4 v[110:113], v[158:159], off offset:3072
	ds_read_b64_tr_b16 v[156:157], v189 offset:0x2080
	ds_read_b64_tr_b16 v[158:159], v189 offset:0x2280
	ds_read_b64_tr_b16 v[164:165], v189 offset:0x2480
	ds_read_b64_tr_b16 v[166:167], v189 offset:0x2680
	ds_read_b64_tr_b16 v[168:169], v189 offset:0x28a0
	ds_read_b64_tr_b16 v[170:171], v189 offset:0x2aa0
	ds_read_b64_tr_b16 v[172:173], v189 offset:0x2ca0
	ds_read_b64_tr_b16 v[174:175], v189 offset:0x2ea0
	ds_read_b64_tr_b16 v[200:201], v189 offset:0x30c0
	ds_read_b64_tr_b16 v[202:203], v189 offset:0x32c0
	ds_read_b64_tr_b16 v[204:205], v189 offset:0x34c0
	ds_read_b64_tr_b16 v[206:207], v189 offset:0x36c0
	s_waitcnt lgkmcnt(4)
	s_nop 0
	v_mfma_f32_16x16x32_bf16 v[54:57], v[156:159], v[114:117], v[54:57]
	v_mfma_f32_16x16x32_bf16 v[62:65], v[156:159], v[118:121], v[62:65]
	v_mfma_f32_16x16x32_bf16 v[58:61], v[168:171], v[114:117], v[58:61]
	v_mfma_f32_16x16x32_bf16 v[70:73], v[168:171], v[118:121], v[70:73]
	v_mfma_f32_16x16x32_bf16 v[54:57], v[164:167], v[122:125], v[54:57]
	v_mfma_f32_16x16x32_bf16 v[62:65], v[164:167], v[126:129], v[62:65]
	v_mfma_f32_16x16x32_bf16 v[58:61], v[172:175], v[122:125], v[58:61]
	v_mfma_f32_16x16x32_bf16 v[70:73], v[172:175], v[126:129], v[70:73]
	ds_read_b64_tr_b16 v[156:157], v189 offset:0x38e0
	ds_read_b64_tr_b16 v[158:159], v189 offset:0x3ae0
	ds_read_b64_tr_b16 v[164:165], v189 offset:0x3ce0
	ds_read_b64_tr_b16 v[166:167], v189 offset:0x3ee0
	s_waitcnt lgkmcnt(4)
	v_mfma_f32_16x16x32_bf16 v[42:45], v[200:203], v[114:117], v[42:45]
	s_waitcnt lgkmcnt(0)
	v_mfma_f32_16x16x32_bf16 v[46:49], v[200:203], v[118:121], v[46:49]
	v_mfma_f32_16x16x32_bf16 v[42:45], v[204:207], v[122:125], v[42:45]
	v_mfma_f32_16x16x32_bf16 v[46:49], v[204:207], v[126:129], v[46:49]
	v_mfma_f32_16x16x32_bf16 v[66:69], v[156:159], v[114:117], v[66:69]
	v_mfma_f32_16x16x32_bf16 v[74:77], v[156:159], v[118:121], v[74:77]
	v_mfma_f32_16x16x32_bf16 v[66:69], v[164:167], v[122:125], v[66:69]
	v_mfma_f32_16x16x32_bf16 v[74:77], v[164:167], v[126:129], v[74:77]
	v_exp_f32_e32 v158, v196
	v_exp_f32_e32 v152, v197
	v_exp_f32_e32 v156, v198
	v_exp_f32_e32 v160, v199
	v_exp_f32_e32 v159, v220
	v_exp_f32_e32 v153, v221
	v_exp_f32_e32 v157, v222
	v_exp_f32_e32 v161, v223
	v_exp_f32_e32 v168, v224
	v_exp_f32_e32 v170, v225
	v_exp_f32_e32 v164, v226
	v_exp_f32_e32 v166, v227
	v_exp_f32_e32 v169, v146
	v_exp_f32_e32 v171, v147
	v_exp_f32_e32 v165, v148
	v_exp_f32_e32 v167, v149
	v_exp_f32_e32 v142, v142
	v_exp_f32_e32 v172, v143
	v_exp_f32_e32 v144, v144
	v_exp_f32_e32 v174, v145
	v_exp_f32_e32 v143, v138
	v_exp_f32_e32 v173, v139
	v_exp_f32_e32 v145, v140
	v_exp_f32_e32 v175, v141
	v_exp_f32_e32 v134, v134
	v_exp_f32_e32 v138, v135
	v_exp_f32_e32 v136, v136
	v_exp_f32_e32 v140, v137
	v_exp_f32_e32 v135, v130
	v_exp_f32_e32 v139, v131
	v_exp_f32_e32 v137, v132
	v_exp_f32_e32 v141, v133
	s_add_u32 s14, s14, 0x90000
	s_addc_u32 s15, s15, 0
	s_cmp_lg_u32 s14, 0x9120000
	s_mov_b32 s16, s17
	s_cbranch_scc1 .LBB0_650
	s_waitcnt vmcnt(1)
	v_cvt_pk_bf16_f32 v106, v158, v152
	v_cvt_pk_bf16_f32 v107, v156, v160
	v_cvt_pk_bf16_f32 v108, v168, v170
	v_cvt_pk_bf16_f32 v109, v164, v166
	s_waitcnt vmcnt(0)
	v_cvt_pk_bf16_f32 v110, v159, v153
	v_cvt_pk_bf16_f32 v111, v157, v161
	v_cvt_pk_bf16_f32 v112, v169, v171
	v_cvt_pk_bf16_f32 v113, v165, v167
	v_cvt_pk_bf16_f32 v114, v142, v172
	v_cvt_pk_bf16_f32 v115, v144, v174
	v_cvt_pk_bf16_f32 v116, v134, v138
	v_cvt_pk_bf16_f32 v117, v136, v140
	v_cvt_pk_bf16_f32 v118, v143, v173
	v_cvt_pk_bf16_f32 v119, v145, v175
	v_cvt_pk_bf16_f32 v120, v135, v139
	v_cvt_pk_bf16_f32 v121, v137, v141
	s_waitcnt lgkmcnt(0)
	s_barrier
; #define SBAR() __builtin_amdgcn_sched_barrier(0)
; #define HLOADV(kt) do { const char* vb_ = (const char*)Vh + (size_t)(kt) * (64 * LDK * 2); sv0 = *(const bf16x8*)(vb_ + koff0); sv1 = *(const bf16x8*)(vb_ + koff1); } while (0)
; #define HLOADK(kt) do { const char* kb_ = (const char*)Kh + (size_t)(kt) * (64 * LDK * 2); sk0 = *(const bf16x8*)(kb_ + koff0); sk1 = *(const bf16x8*)(kb_ + koff1); } while (0)
; #define HWRITEV(b) do { char* d_ = V_lds + (b) * G16_V; *(bf16x8*)(d_ + vst0) = sv0; *(bf16x8*)(d_ + vst1) = sv1; } while (0)
; #define HWRITEK(b) do { char* d_ = K_lds + (b) * GB_K; *(bf16x8*)(d_ + KSWZ(sr, sc * 2)) = sk0; *(bf16x8*)(d_ + KSWZ(32 + sr, sc * 2)) = sk1; } while (0)
; #define HEXP() do { _Pragma("unroll") for (int kt = 0; kt < 4; ++kt) { _Pragma("unroll") for (int qt = 0; qt < 2; ++qt) { _Pragma("unroll") for (int i = 0; i < 4; ++i) s[kt][qt][i] = __builtin_amdgcn_exp2f(fmaf(s[kt][qt][i], C, mnC)); } } } while (0)
; template <int LDQ, int LDK, int LDO>
; __device__ __forceinline__ void attn_gqa16_body(const bf16* __restrict__ Qb, const bf16* __restrict__ Kh, const bf16* __restrict__ Vh, bf16* __restrict__ Ob, int seq, char* lds, float mref) {
;     ...
;   const int NT = seq / KVBLK;
;   HLOADK(0); HLOADV(0); asm volatile("s_waitcnt vmcnt(0)" ::: "memory"); HWRITEK(0); HWRITEV(0);
;   HLOADK(1); asm volatile("s_waitcnt vmcnt(0)" ::: "memory"); HWRITEK(1); __syncthreads();
;   HLOADK(2); HLOADV(1);
;   HQK(0); HEXP();
;   if (wid >= 4) __builtin_amdgcn_s_setprio(1);
;   for (int t = 0; t < NT; ++t) {
;     HPACK();
;     __syncthreads();
;     const bool more = t + 1 < NT;
;     if (more) HQK((t + 1) & 1);
;     const int vb = vb0 + (t & 1) * (int)G16_V;
;     SBAR(); pv16<0>(o, vb, pb); SBAR();
	s_mov_b32 m0, s86
	s_nop 0
	global_load_lds_dwordx4 v253, s[74:75]
	s_add_i32 m0, s86, 0x400
	s_nop 0
	global_load_lds_dwordx4 v253, s[76:77]
	ds_read_b128 v[122:125], v182 offset:50688
	ds_read_b128 v[126:129], v182 offset:50752
	ds_read_b128 v[146:149], v182 offset:55040
	ds_read_b128 v[196:199], v182 offset:55104
	ds_read_b128 v[204:207], v182 offset:59392
	ds_read_b128 v[208:211], v182 offset:59456
	ds_read_b128 v[216:219], v182 offset:63744
	ds_read_b128 v[220:223], v182 offset:63808
	s_waitcnt lgkmcnt(7)
	v_mfma_f32_16x16x32_bf16 v[130:133], v[122:125], v[30:33], 0
	v_mov_b32_e32 v190, v168
	v_mov_b32_e32 v191, v158
	v_mov_b32_e32 v192, v170
	v_mfma_f32_16x16x32_bf16 v[122:125], v[122:125], v[38:41], 0
	v_mov_b32_e32 v193, v152
	v_mov_b32_e32 v152, v171
	s_lshl_b32 s8, s8, 12
	s_waitcnt lgkmcnt(5)
	v_mfma_f32_16x16x32_bf16 v[200:203], v[146:149], v[30:33], 0
	s_add_u32 s8, s42, s8
	s_addc_u32 s14, s43, 0
	s_add_u32 s12, s8, s12
	v_mfma_f32_16x16x32_bf16 v[146:149], v[146:149], v[38:41], 0
	s_addc_u32 s13, s14, s13
	s_waitcnt lgkmcnt(3)
	v_mfma_f32_16x16x32_bf16 v[212:215], v[204:207], v[30:33], 0
	s_waitcnt lgkmcnt(1)
	v_mfma_f32_16x16x32_bf16 v[30:33], v[216:219], v[30:33], 0
	v_mfma_f32_16x16x32_bf16 v[130:133], v[126:129], v[18:21], v[130:133]
	v_mfma_f32_16x16x32_bf16 v[122:125], v[126:129], v[22:25], v[122:125]
	v_mfma_f32_16x16x32_bf16 v[126:129], v[196:199], v[18:21], v[200:203]
	v_mfma_f32_16x16x32_bf16 v[146:149], v[196:199], v[22:25], v[146:149]
	v_mfma_f32_16x16x32_bf16 v[196:199], v[208:211], v[18:21], v[212:215]
	s_waitcnt lgkmcnt(0)
	v_mfma_f32_16x16x32_bf16 v[18:21], v[220:223], v[18:21], v[30:33]
	s_nop 0
	v_mov_b32_e32 v213, v156
	v_mov_b32_e32 v212, v164
	v_mov_b32_e32 v214, v166
	ds_read_b128 v[30:33], v182 offset:50816
	v_mfma_f32_16x16x32_bf16 v[204:207], v[204:207], v[38:41], 0
	v_mov_b32_e32 v215, v160
	v_mfma_f32_16x16x32_bf16 v[38:41], v[216:219], v[38:41], 0
	v_mov_b32_e32 v216, v169
	v_mov_b32_e32 v217, v159
	v_mov_b32_e32 v219, v157
	v_mfma_f32_16x16x32_bf16 v[200:203], v[208:211], v[22:25], v[204:207]
	v_mov_b32_e32 v218, v165
	v_mfma_f32_16x16x32_bf16 v[22:25], v[220:223], v[22:25], v[38:41]
	s_nop 2
	ds_read_b128 v[38:41], v182 offset:55168
	ds_read_b128 v[204:207], v182 offset:50880
	s_waitcnt lgkmcnt(2)
	v_mfma_f32_16x16x32_bf16 v[130:133], v[30:33], v[10:13], v[130:133]
	v_mfma_f32_16x16x32_bf16 v[30:33], v[30:33], v[14:17], v[122:125]
	s_nop 2
	ds_read_b128 v[122:125], v182 offset:59520
	ds_read_b128 v[208:211], v182 offset:55232
	s_waitcnt lgkmcnt(3)
	v_mfma_f32_16x16x32_bf16 v[126:129], v[38:41], v[10:13], v[126:129]
	v_mfma_f32_16x16x32_bf16 v[38:41], v[38:41], v[14:17], v[146:149]
	s_nop 2
	ds_read_b128 v[146:149], v182 offset:63872
	ds_read_b128 v[168:171], v182 offset:59584
	ds_read_b128 v[156:159], v182 offset:63936
	s_waitcnt lgkmcnt(4)
	v_mfma_f32_16x16x32_bf16 v[196:199], v[122:125], v[10:13], v[196:199]
	s_waitcnt lgkmcnt(2)
	v_mfma_f32_16x16x32_bf16 v[10:13], v[146:149], v[10:13], v[18:21]
	v_mfma_f32_16x16x32_bf16 v[122:125], v[122:125], v[14:17], v[200:203]
	s_nop 1
	v_mov_b32_e32 v18, v142
	v_mov_b32_e32 v19, v144
	v_mov_b32_e32 v20, v172
	v_mfma_f32_16x16x32_bf16 v[14:17], v[146:149], v[14:17], v[22:25]
	v_mov_b32_e32 v201, v161
	v_mov_b32_e32 v200, v167
	v_mov_b32_e32 v21, v174
	v_mfma_f32_16x16x32_bf16 v[160:163], v[204:207], v[6:9], v[30:33]
	v_add_f32_e64 v24, v190, v192
	v_add_f32_e64 v25, v191, v193
	v_mov_b32_e32 v144, v143
	v_mov_b32_e32 v22, v173
	v_pk_add_f32 v[30:31], v[212:213], v[214:215]
	v_mfma_f32_16x16x32_bf16 v[146:149], v[204:207], v[2:5], v[130:133]
	v_add_f32_e64 v24, v24, v30
	v_add_f32_e64 v25, v25, v31
	v_mov_b32_e32 v23, v175
	v_pk_add_f32 v[32:33], v[216:217], v[152:153]
	v_mfma_f32_16x16x32_bf16 v[164:167], v[208:211], v[2:5], v[126:129]
	v_add_f32_e64 v144, v144, v22
	v_add_f32_e64 v145, v145, v23
	v_add_f32_e32 v130, v134, v138
	v_add_f32_e32 v132, v136, v140
	v_mfma_f32_16x16x32_bf16 v[172:175], v[208:211], v[6:9], v[38:41]
	v_add_f32_e64 v126, v18, v20
	v_add_f32_e64 v127, v19, v21
	s_nop 0
	v_pk_add_f32 v[38:39], v[218:219], v[200:201]
	s_waitcnt lgkmcnt(1)
	v_mfma_f32_16x16x32_bf16 v[196:199], v[168:171], v[2:5], v[196:199]
	v_add_f32_e64 v142, v32, v38
	v_add_f32_e64 v143, v33, v39
	s_waitcnt lgkmcnt(0)
	v_mfma_f32_16x16x32_bf16 v[200:203], v[156:159], v[2:5], v[10:13]
	v_add_f32_e64 v2, v150, v25
	v_add_f32_e64 v3, v151, v24
	v_pk_add_f32 v[128:129], v[24:25], v[2:3]
	v_mfma_f32_16x16x32_bf16 v[168:171], v[168:171], v[6:9], v[122:125]
	s_nop 2
	v_add_f32_e32 v122, v135, v139
	v_add_f32_e32 v124, v137, v141
	v_mfma_f32_16x16x32_bf16 v[134:137], v[156:159], v[6:9], v[14:17]
	ds_read_b64_tr_b16 v[2:3], v183 offset:0
	ds_read_b64_tr_b16 v[4:5], v183 offset:0x200
	ds_read_b64_tr_b16 v[6:7], v183 offset:0x400
	ds_read_b64_tr_b16 v[8:9], v183 offset:0x600
	ds_read_b64_tr_b16 v[10:11], v183 offset:0x820
	ds_read_b64_tr_b16 v[12:13], v183 offset:0xa20
	ds_read_b64_tr_b16 v[14:15], v183 offset:0xc20
	ds_read_b64_tr_b16 v[16:17], v183 offset:0xe20
	ds_read_b64_tr_b16 v[18:19], v183 offset:0x1040
	ds_read_b64_tr_b16 v[20:21], v183 offset:0x1240
	ds_read_b64_tr_b16 v[22:23], v183 offset:0x1440
	ds_read_b64_tr_b16 v[24:25], v183 offset:0x1640
	s_waitcnt lgkmcnt(4)
	s_nop 0
	v_mfma_f32_16x16x32_bf16 v[30:33], v[2:5], v[106:109], v[102:105]
	v_mfma_f32_16x16x32_bf16 v[38:41], v[2:5], v[110:113], v[98:101]
	v_mfma_f32_16x16x32_bf16 v[94:97], v[10:13], v[106:109], v[94:97]
	v_mfma_f32_16x16x32_bf16 v[10:13], v[10:13], v[110:113], v[90:93]
	v_mfma_f32_16x16x32_bf16 v[2:5], v[6:9], v[114:117], v[30:33]
	v_mfma_f32_16x16x32_bf16 v[6:9], v[6:9], v[118:121], v[38:41]
	v_mfma_f32_16x16x32_bf16 v[38:41], v[14:17], v[114:117], v[94:97]
	v_mfma_f32_16x16x32_bf16 v[90:93], v[14:17], v[118:121], v[10:13]
	ds_read_b64_tr_b16 v[14:15], v183 offset:0x1860
	ds_read_b64_tr_b16 v[16:17], v183 offset:0x1a60
	ds_read_b64_tr_b16 v[30:31], v183 offset:0x1c60
	ds_read_b64_tr_b16 v[32:33], v183 offset:0x1e60
	s_waitcnt lgkmcnt(4)
; #define SBAR() __builtin_amdgcn_sched_barrier(0)
; #define MFMA16(a, b, c) __builtin_amdgcn_mfma_f32_16x16x32_bf16(a, b, c, 0, 0, 0)
; template <int D0> __device__ __forceinline__ void pv16(f32x4a (&o)[8][2], int vb, const bf16x8 (&pb)[2][2]) {
;     ...
;   const s16x4 a0 = TR(D0, 0, 0), a1 = TR(D0, 0, 1), a2 = TR(D0, 1, 0), a3 = TR(D0, 1, 1), b0 = TR(D0 + 1, 0, 0), b1 = TR(D0 + 1, 0, 1), b2 = TR(D0 + 1, 1, 0), b3 = TR(D0 + 1, 1, 1);
;   const s16x4 c0 = TR(D0 + 2, 0, 0), c1 = TR(D0 + 2, 0, 1), c2 = TR(D0 + 2, 1, 0), c3 = TR(D0 + 2, 1, 1);
;   asm volatile("s_waitcnt lgkmcnt(4)" ::: "memory"); SBAR();
;   o[D0][0] = MFMA16(PK16(a0, a1), pb[0][0], o[D0][0]); o[D0][1] = MFMA16(PK16(a0, a1), pb[0][1], o[D0][1]);
;   o[D0 + 1][0] = MFMA16(PK16(b0, b1), pb[0][0], o[D0 + 1][0]); o[D0 + 1][1] = MFMA16(PK16(b0, b1), pb[0][1], o[D0 + 1][1]);
;   o[D0][0] = MFMA16(PK16(a2, a3), pb[1][0], o[D0][0]); o[D0][1] = MFMA16(PK16(a2, a3), pb[1][1], o[D0][1]);
;   o[D0 + 1][0] = MFMA16(PK16(b2, b3), pb[1][0], o[D0 + 1][0]); o[D0 + 1][1] = MFMA16(PK16(b2, b3), pb[1][1], o[D0 + 1][1]);
;   SBAR();
;   const s16x4 d0 = TR(D0 + 3, 0, 0), d1 = TR(D0 + 3, 0, 1), d2 = TR(D0 + 3, 1, 0), d3 = TR(D0 + 3, 1, 1);
;   asm volatile("s_waitcnt lgkmcnt(4)" ::: "memory"); SBAR();
;   o[D0 + 2][0] = MFMA16(PK16(c0, c1), pb[0][0], o[D0 + 2][0]); o[D0 + 2][1] = MFMA16(PK16(c0, c1), pb[0][1], o[D0 + 2][1]);
;   o[D0 + 2][0] = MFMA16(PK16(c2, c3), pb[1][0], o[D0 + 2][0]); o[D0 + 2][1] = MFMA16(PK16(c2, c3), pb[1][1], o[D0 + 2][1]);
;   asm volatile("s_waitcnt lgkmcnt(0)" ::: "memory"); SBAR();
;   o[D0 + 3][0] = MFMA16(PK16(d0, d1), pb[0][0], o[D0 + 3][0]); o[D0 + 3][1] = MFMA16(PK16(d0, d1), pb[0][1], o[D0 + 3][1]);
;   o[D0 + 3][0] = MFMA16(PK16(d2, d3), pb[1][0], o[D0 + 3][0]); o[D0 + 3][1] = MFMA16(PK16(d2, d3), pb[1][1], o[D0 + 3][1]);
	v_mfma_f32_16x16x32_bf16 v[10:13], v[18:21], v[106:109], v[78:81]
	s_waitcnt lgkmcnt(0)
	v_mfma_f32_16x16x32_bf16 v[18:21], v[18:21], v[110:113], v[50:53]
	v_mfma_f32_16x16x32_bf16 v[10:13], v[22:25], v[114:117], v[10:13]
	v_mfma_f32_16x16x32_bf16 v[22:25], v[22:25], v[118:121], v[18:21]
	v_mfma_f32_16x16x32_bf16 v[18:21], v[14:17], v[106:109], v[82:85]
	v_mfma_f32_16x16x32_bf16 v[50:53], v[14:17], v[110:113], v[86:89]
	v_mfma_f32_16x16x32_bf16 v[14:17], v[30:33], v[114:117], v[18:21]
	v_mfma_f32_16x16x32_bf16 v[18:21], v[30:33], v[118:121], v[50:53]
	s_waitcnt vmcnt(0)
	s_waitcnt vmcnt(1)
	s_waitcnt vmcnt(0)
	ds_read_b64_tr_b16 v[26:27], v183 offset:0x2080
	ds_read_b64_tr_b16 v[28:29], v183 offset:0x2280
	ds_read_b64_tr_b16 v[30:31], v183 offset:0x2480
	ds_read_b64_tr_b16 v[32:33], v183 offset:0x2680
	ds_read_b64_tr_b16 v[34:35], v183 offset:0x28a0
	ds_read_b64_tr_b16 v[36:37], v183 offset:0x2aa0
	ds_read_b64_tr_b16 v[78:79], v183 offset:0x2ca0
	ds_read_b64_tr_b16 v[80:81], v183 offset:0x2ea0
	ds_read_b64_tr_b16 v[82:83], v183 offset:0x30c0
	ds_read_b64_tr_b16 v[84:85], v183 offset:0x32c0
	ds_read_b64_tr_b16 v[86:87], v183 offset:0x34c0
	ds_read_b64_tr_b16 v[88:89], v183 offset:0x36c0
	s_waitcnt lgkmcnt(4)
	s_nop 0
	v_mfma_f32_16x16x32_bf16 v[50:53], v[26:29], v[106:109], v[54:57]
	v_mfma_f32_16x16x32_bf16 v[26:29], v[26:29], v[110:113], v[62:65]
	v_mfma_f32_16x16x32_bf16 v[58:61], v[34:37], v[106:109], v[58:61]
	v_mfma_f32_16x16x32_bf16 v[34:37], v[34:37], v[110:113], v[70:73]
	v_mfma_f32_16x16x32_bf16 v[50:53], v[30:33], v[114:117], v[50:53]
	v_mfma_f32_16x16x32_bf16 v[54:57], v[30:33], v[118:121], v[26:29]
	v_mfma_f32_16x16x32_bf16 v[70:73], v[78:81], v[114:117], v[58:61]
	v_mfma_f32_16x16x32_bf16 v[78:81], v[78:81], v[118:121], v[34:37]
	ds_read_b64_tr_b16 v[30:31], v183 offset:0x38e0
	ds_read_b64_tr_b16 v[32:33], v183 offset:0x3ae0
	ds_read_b64_tr_b16 v[34:35], v183 offset:0x3ce0
	ds_read_b64_tr_b16 v[36:37], v183 offset:0x3ee0
	s_waitcnt lgkmcnt(4)
	v_mfma_f32_16x16x32_bf16 v[26:29], v[82:85], v[106:109], v[42:45]
	s_waitcnt lgkmcnt(0)
	v_mfma_f32_16x16x32_bf16 v[42:45], v[82:85], v[110:113], v[46:49]
	v_mfma_f32_16x16x32_bf16 v[26:29], v[86:89], v[114:117], v[26:29]
	v_mfma_f32_16x16x32_bf16 v[58:61], v[86:89], v[118:121], v[42:45]
	v_mfma_f32_16x16x32_bf16 v[42:45], v[30:33], v[106:109], v[66:69]
	v_mfma_f32_16x16x32_bf16 v[46:49], v[30:33], v[110:113], v[74:77]
	v_mfma_f32_16x16x32_bf16 v[30:33], v[34:37], v[114:117], v[42:45]
	v_mfma_f32_16x16x32_bf16 v[62:65], v[34:37], v[118:121], v[46:49]
	s_nop 4
	v_add_f32_e32 v42, v186, v196
	v_exp_f32_e32 v116, v42
	v_add_f32_e32 v42, v186, v197
	v_exp_f32_e32 v117, v42
	v_add_f32_e32 v42, v186, v198
	v_exp_f32_e32 v118, v42
	v_add_f32_e32 v42, v186, v199
	v_exp_f32_e32 v119, v42
	v_add_f32_e32 v42, v186, v168
	v_add_f32_e32 v34, v186, v146
	v_exp_f32_e32 v98, v42
	v_add_f32_e32 v42, v186, v169
	v_exp_f32_e32 v131, v34
	v_add_f32_e32 v34, v186, v147
	v_exp_f32_e32 v99, v42
	v_add_f32_e32 v42, v186, v170
	v_exp_f32_e32 v133, v34
	v_add_f32_e32 v34, v186, v148
	v_exp_f32_e32 v100, v42
	v_add_f32_e32 v42, v186, v171
	v_exp_f32_e32 v74, v34
	v_add_f32_e32 v34, v186, v149
	v_exp_f32_e32 v101, v42
	v_add_f32_e32 v42, v186, v200
	v_exp_f32_e32 v129, v34
	v_add_f32_e32 v34, v186, v160
	v_exp_f32_e32 v120, v42
	v_add_f32_e32 v42, v186, v201
	v_exp_f32_e32 v123, v34
	v_add_f32_e32 v34, v186, v161
	v_exp_f32_e32 v121, v42
	v_add_f32_e32 v42, v186, v202
	v_exp_f32_e32 v125, v34
	v_add_f32_e32 v34, v186, v162
	v_exp_f32_e32 v75, v42
	v_add_f32_e32 v42, v186, v203
	v_exp_f32_e32 v76, v34
	v_add_f32_e32 v34, v186, v163
	v_exp_f32_e32 v77, v42
	v_add_f32_e32 v42, v186, v134
	v_exp_f32_e32 v87, v34
	v_add_f32_e32 v34, v186, v164
	v_exp_f32_e32 v102, v42
	v_add_f32_e32 v42, v186, v135
	v_exp_f32_e32 v66, v34
	v_add_f32_e32 v34, v186, v165
	v_exp_f32_e32 v103, v42
	v_add_f32_e32 v42, v186, v136
	v_exp_f32_e32 v68, v34
	v_add_f32_e32 v34, v186, v166
	v_exp_f32_e32 v43, v42
	v_exp_f32_e32 v67, v34
	v_add_f32_e32 v34, v186, v167
	v_add_f32_e32 v35, v186, v173
	v_exp_f32_e32 v69, v34
	v_add_f32_e32 v34, v186, v172
	v_exp_f32_e32 v36, v35
	v_add_f32_e32 v35, v186, v174
	v_add_f32_e32 v37, v186, v175
	v_add_f32_e32 v42, v186, v137
	v_exp_f32_e32 v34, v34
	v_exp_f32_e32 v35, v35
	v_exp_f32_e32 v37, v37
	v_exp_f32_e32 v45, v42
	v_add_f32_e32 v42, v143, v151
	v_pk_add_f32 v[48:49], v[144:145], v[144:145] op_sel:[0,1] op_sel_hi:[1,0]
	v_pk_add_f32 v[84:85], v[142:143], v[42:43] op_sel_hi:[1,0]
	v_mov_b32_e32 v49, v76
	v_mov_b32_e32 v85, v87
	v_pk_add_f32 v[46:47], v[122:123], v[124:125]
	v_pk_add_f32 v[48:49], v[48:49], v[84:85]
	v_add_f32_e32 v42, v98, v99
	v_pk_add_f32 v[46:47], v[46:47], v[48:49]
	v_pk_add_f32 v[48:49], v[34:35], v[36:37]
	v_pk_add_f32 v[46:47], v[46:47], v[46:47] op_sel:[0,1] op_sel_hi:[1,0]
	v_pk_add_f32 v[48:49], v[48:49], v[48:49] op_sel:[0,1] op_sel_hi:[1,0]
	v_add_f32_e32 v44, v100, v101
	v_mov_b32_e32 v47, v102
	v_mov_b32_e32 v49, v103
	v_pk_add_f32 v[46:47], v[46:47], v[48:49]
	v_pk_add_f32 v[48:49], v[42:43], v[44:45]
	v_cvt_pk_bf16_f32 v82, v131, v133
	v_cvt_pk_bf16_f32 v83, v74, v129
	v_cvt_pk_bf16_f32 v84, v66, v68
	v_cvt_pk_bf16_f32 v85, v67, v69
	v_cvt_pk_bf16_f32 v86, v123, v125
	s_nop 0
	v_pk_add_f32 v[46:47], v[46:47], v[48:49]
	v_pk_add_f32 v[48:49], v[126:127], v[126:127] op_sel:[0,1] op_sel_hi:[1,0]
	v_add_f32_e32 v122, v46, v47
	v_mov_b32_e32 v49, v74
	v_pk_add_f32 v[46:47], v[130:131], v[132:133]
	v_pk_add_f32 v[48:49], v[48:49], v[128:129]
	v_cvt_pk_bf16_f32 v87, v76, v87
	v_cvt_pk_bf16_f32 v88, v34, v36
	v_cvt_pk_bf16_f32 v89, v35, v37
	v_cvt_pk_bf16_f32 v94, v116, v117
	v_cvt_pk_bf16_f32 v95, v118, v119
	s_nop 0
	v_pk_add_f32 v[114:115], v[46:47], v[48:49]
	v_cvt_pk_bf16_f32 v96, v120, v121
	v_cvt_pk_bf16_f32 v97, v75, v77
	v_cvt_pk_bf16_f32 v98, v98, v99
	v_cvt_pk_bf16_f32 v99, v100, v101
	v_cvt_pk_bf16_f32 v100, v102, v103
	v_cvt_pk_bf16_f32 v101, v43, v45
	s_waitcnt lgkmcnt(0)
	s_barrier
; #define SBAR() __builtin_amdgcn_sched_barrier(0)
; #define MFMA16(a, b, c) __builtin_amdgcn_mfma_f32_16x16x32_bf16(a, b, c, 0, 0, 0)
; template <int D0> __device__ __forceinline__ void pv16(f32x4a (&o)[8][2], int vb, const bf16x8 (&pb)[2][2]) {
;     ...
;   const s16x4 a0 = TR(D0, 0, 0), a1 = TR(D0, 0, 1), a2 = TR(D0, 1, 0), a3 = TR(D0, 1, 1), b0 = TR(D0 + 1, 0, 0), b1 = TR(D0 + 1, 0, 1), b2 = TR(D0 + 1, 1, 0), b3 = TR(D0 + 1, 1, 1);
;   const s16x4 c0 = TR(D0 + 2, 0, 0), c1 = TR(D0 + 2, 0, 1), c2 = TR(D0 + 2, 1, 0), c3 = TR(D0 + 2, 1, 1);
;   asm volatile("s_waitcnt lgkmcnt(4)" ::: "memory"); SBAR();
;   o[D0][0] = MFMA16(PK16(a0, a1), pb[0][0], o[D0][0]); o[D0][1] = MFMA16(PK16(a0, a1), pb[0][1], o[D0][1]);
;   o[D0 + 1][0] = MFMA16(PK16(b0, b1), pb[0][0], o[D0 + 1][0]); o[D0 + 1][1] = MFMA16(PK16(b0, b1), pb[0][1], o[D0 + 1][1]);
;   o[D0][0] = MFMA16(PK16(a2, a3), pb[1][0], o[D0][0]); o[D0][1] = MFMA16(PK16(a2, a3), pb[1][1], o[D0][1]);
;   o[D0 + 1][0] = MFMA16(PK16(b2, b3), pb[1][0], o[D0 + 1][0]); o[D0 + 1][1] = MFMA16(PK16(b2, b3), pb[1][1], o[D0 + 1][1]);
;   SBAR();
;   const s16x4 d0 = TR(D0 + 3, 0, 0), d1 = TR(D0 + 3, 0, 1), d2 = TR(D0 + 3, 1, 0), d3 = TR(D0 + 3, 1, 1);
;   asm volatile("s_waitcnt lgkmcnt(4)" ::: "memory"); SBAR();
;   o[D0 + 2][0] = MFMA16(PK16(c0, c1), pb[0][0], o[D0 + 2][0]); o[D0 + 2][1] = MFMA16(PK16(c0, c1), pb[0][1], o[D0 + 2][1]);
;   o[D0 + 2][0] = MFMA16(PK16(c2, c3), pb[1][0], o[D0 + 2][0]); o[D0 + 2][1] = MFMA16(PK16(c2, c3), pb[1][1], o[D0 + 2][1]);
;   asm volatile("s_waitcnt lgkmcnt(0)" ::: "memory"); SBAR();
;   o[D0 + 3][0] = MFMA16(PK16(d0, d1), pb[0][0], o[D0 + 3][0]); o[D0 + 3][1] = MFMA16(PK16(d0, d1), pb[0][1], o[D0 + 3][1]);
;   o[D0 + 3][0] = MFMA16(PK16(d2, d3), pb[1][0], o[D0 + 3][0]); o[D0 + 3][1] = MFMA16(PK16(d2, d3), pb[1][1], o[D0 + 3][1]);
; template <int LDQ, int LDK, int LDO>
; __device__ __forceinline__ void attn_gqa16_body(const bf16* __restrict__ Qb, const bf16* __restrict__ Kh, const bf16* __restrict__ Vh, bf16* __restrict__ Ob, int seq, char* lds, float mref) {
;     ...
;     SBAR(); pv16<4>(o, vb, pb); SBAR();
;     if (more) HEXP();
;   }
;   __builtin_amdgcn_s_setprio(0);
;   ls0 += __shfl_xor(ls0, 16); ls0 += __shfl_xor(ls0, 32); ls1 += __shfl_xor(ls1, 16); ls1 += __shfl_xor(ls1, 32);
;   const float rl[2] = {__builtin_amdgcn_rcpf(ls0), __builtin_amdgcn_rcpf(ls1)};
	ds_read_b64_tr_b16 v[34:35], v184 offset:0
	ds_read_b64_tr_b16 v[36:37], v184 offset:0x200
	ds_read_b64_tr_b16 v[42:43], v184 offset:0x400
	ds_read_b64_tr_b16 v[44:45], v184 offset:0x600
	ds_read_b64_tr_b16 v[46:47], v184 offset:0x820
	ds_read_b64_tr_b16 v[48:49], v184 offset:0xa20
	ds_read_b64_tr_b16 v[102:103], v184 offset:0xc20
	ds_read_b64_tr_b16 v[104:105], v184 offset:0xe20
	ds_read_b64_tr_b16 v[106:107], v184 offset:0x1040
	ds_read_b64_tr_b16 v[108:109], v184 offset:0x1240
	ds_read_b64_tr_b16 v[110:111], v184 offset:0x1440
	ds_read_b64_tr_b16 v[112:113], v184 offset:0x1640
	s_waitcnt lgkmcnt(4)
	s_nop 0
	v_mfma_f32_16x16x32_bf16 v[2:5], v[34:37], v[82:85], v[2:5]
	v_mfma_f32_16x16x32_bf16 v[6:9], v[34:37], v[86:89], v[6:9]
	v_mfma_f32_16x16x32_bf16 v[34:37], v[46:49], v[82:85], v[38:41]
	v_mfma_f32_16x16x32_bf16 v[46:49], v[46:49], v[86:89], v[90:93]
	v_mfma_f32_16x16x32_bf16 v[38:41], v[42:45], v[94:97], v[2:5]
	v_mfma_f32_16x16x32_bf16 v[6:9], v[42:45], v[98:101], v[6:9]
	v_mfma_f32_16x16x32_bf16 v[34:37], v[102:105], v[94:97], v[34:37]
	v_mfma_f32_16x16x32_bf16 v[2:5], v[102:105], v[98:101], v[46:49]
	ds_read_b64_tr_b16 v[46:47], v184 offset:0x1860
	ds_read_b64_tr_b16 v[48:49], v184 offset:0x1a60
	ds_read_b64_tr_b16 v[90:91], v184 offset:0x1c60
	ds_read_b64_tr_b16 v[92:93], v184 offset:0x1e60
	s_waitcnt lgkmcnt(4)
	v_mfma_f32_16x16x32_bf16 v[10:13], v[106:109], v[82:85], v[10:13]
	s_waitcnt lgkmcnt(0)
	v_mfma_f32_16x16x32_bf16 v[22:25], v[106:109], v[86:89], v[22:25]
	v_mfma_f32_16x16x32_bf16 v[42:45], v[110:113], v[94:97], v[10:13]
	v_mfma_f32_16x16x32_bf16 v[10:13], v[110:113], v[98:101], v[22:25]
	v_mfma_f32_16x16x32_bf16 v[14:17], v[46:49], v[82:85], v[14:17]
	v_mfma_f32_16x16x32_bf16 v[18:21], v[46:49], v[86:89], v[18:21]
	v_mfma_f32_16x16x32_bf16 v[46:49], v[90:93], v[94:97], v[14:17]
	v_mfma_f32_16x16x32_bf16 v[14:17], v[90:93], v[98:101], v[18:21]
	s_waitcnt vmcnt(0)
	ds_read_b64_tr_b16 v[18:19], v184 offset:0x2080
	ds_read_b64_tr_b16 v[20:21], v184 offset:0x2280
	ds_read_b64_tr_b16 v[22:23], v184 offset:0x2480
	ds_read_b64_tr_b16 v[24:25], v184 offset:0x2680
	ds_read_b64_tr_b16 v[90:91], v184 offset:0x28a0
	ds_read_b64_tr_b16 v[92:93], v184 offset:0x2aa0
	ds_read_b64_tr_b16 v[102:103], v184 offset:0x2ca0
	ds_read_b64_tr_b16 v[104:105], v184 offset:0x2ea0
	ds_read_b64_tr_b16 v[106:107], v184 offset:0x30c0
	ds_read_b64_tr_b16 v[108:109], v184 offset:0x32c0
	ds_read_b64_tr_b16 v[110:111], v184 offset:0x34c0
	ds_read_b64_tr_b16 v[112:113], v184 offset:0x36c0
	s_waitcnt lgkmcnt(4)
	s_nop 5
	v_mfma_f32_16x16x32_bf16 v[50:53], v[18:21], v[82:85], v[50:53]
	v_mfma_f32_16x16x32_bf16 v[18:21], v[18:21], v[86:89], v[54:57]
	v_mfma_f32_16x16x32_bf16 v[70:73], v[90:93], v[82:85], v[70:73]
	v_mfma_f32_16x16x32_bf16 v[78:81], v[90:93], v[86:89], v[78:81]
	v_mfma_f32_16x16x32_bf16 v[54:57], v[22:25], v[94:97], v[50:53]
	v_mfma_f32_16x16x32_bf16 v[22:25], v[22:25], v[98:101], v[18:21]
	v_mfma_f32_16x16x32_bf16 v[50:53], v[102:105], v[94:97], v[70:73]
	v_mfma_f32_16x16x32_bf16 v[18:21], v[102:105], v[98:101], v[78:81]
	ds_read_b64_tr_b16 v[70:71], v184 offset:0x38e0
	ds_read_b64_tr_b16 v[72:73], v184 offset:0x3ae0
	ds_read_b64_tr_b16 v[78:79], v184 offset:0x3ce0
	ds_read_b64_tr_b16 v[80:81], v184 offset:0x3ee0
	s_waitcnt lgkmcnt(4)
	v_mfma_f32_16x16x32_bf16 v[26:29], v[106:109], v[82:85], v[26:29]
	s_waitcnt lgkmcnt(0)
	v_mfma_f32_16x16x32_bf16 v[90:93], v[106:109], v[86:89], v[58:61]
	v_mfma_f32_16x16x32_bf16 v[58:61], v[110:113], v[94:97], v[26:29]
	v_mfma_f32_16x16x32_bf16 v[26:29], v[110:113], v[98:101], v[90:93]
	v_mfma_f32_16x16x32_bf16 v[30:33], v[70:73], v[82:85], v[30:33]
	v_mfma_f32_16x16x32_bf16 v[70:73], v[70:73], v[86:89], v[62:65]
	v_mfma_f32_16x16x32_bf16 v[62:65], v[78:81], v[94:97], v[30:33]
	v_mfma_f32_16x16x32_bf16 v[30:33], v[78:81], v[98:101], v[70:73]
	v_add_f32_e64 v66, v66, v68
	v_add_f32_e64 v67, v67, v69
	v_pk_add_f32 v[68:69], v[114:115], v[114:115] op_sel:[0,1] op_sel_hi:[1,0]
	v_pk_add_f32 v[66:67], v[66:67], v[66:67] op_sel:[0,1] op_sel_hi:[1,0]
	v_add_f32_e32 v74, v116, v117
	v_add_f32_e32 v76, v118, v119
	v_mov_b32_e32 v69, v120
	v_mov_b32_e32 v67, v121
	v_pk_add_f32 v[66:67], v[68:69], v[66:67]
	v_pk_add_f32 v[68:69], v[74:75], v[76:77]
	s_nop 0
	v_pk_add_f32 v[66:67], v[66:67], v[68:69]
	s_nop 0
	v_add_f32_e32 v66, v66, v67
	s_setprio 0
	ds_bpermute_b32 v67, v177, v66
	ds_bpermute_b32 v68, v177, v122
	v_mov_b32_e32 v70, v185
	s_waitcnt lgkmcnt(1)
	v_add_f32_e32 v66, v66, v67
	s_waitcnt lgkmcnt(0)
	v_add_f32_e32 v67, v122, v68
	ds_bpermute_b32 v68, v188, v66
	ds_bpermute_b32 v69, v188, v67
	s_waitcnt lgkmcnt(1)
	v_add_f32_e32 v66, v66, v68
	s_waitcnt lgkmcnt(0)
	v_add_f32_e32 v67, v67, v69
	v_rcp_f32_e32 v68, v66
	v_rcp_f32_e32 v66, v67
	v_mov_b32_e32 v67, v176
	v_mov_b32_e32 v69, v180
	s_branch .LBB0_641
